# expert GEMM loops: next-tile address selection hoisted above the landed-tile wait; conversions grouped per load pair so each pair of B loads re-issues as soon as its registers are free
# speedup vs baseline: 1.0053x; 1.0053x over previous
; #define PG8_STAGE_A(bufoff, V0, V1, kb) do { \
;         __builtin_amdgcn_global_load_lds((const unsigned*)((Abase + (kb)) + (V0)), (LAS unsigned*)(lds + (bufoff) + ldsw), 16, 0, 0); \
;         __builtin_amdgcn_global_load_lds((const unsigned*)((Abase + (kb)) + (V1)), (LAS unsigned*)(lds + (bufoff) + ldsw + 8192), 16, 0, 0); } while (0)
; #define PG8_LDA(dst, b, h) do { _Pragma("unroll") for (int m = 0; m < 4; ++m) _Pragma("unroll") for (int k = 0; k < 2; ++k) dst[m][k] = *(const LAS bf16x8*)(lds + PG8_SA(b, h) + aoff + m * 2048 + k * 1024); } while (0)
; #define PG8_LDB(dst, b, h) do { _Pragma("unroll") for (int n = 0; n < 2; ++n) _Pragma("unroll") for (int k = 0; k < 2; ++k) dst[n][k] = *(const LAS bf16x8*)(lds + PG8_SB(b, h) + boff + n * 2048 + k * 1024); } while (0)
; #define PG8_MMA(ai, bj, At, Bt) do { __builtin_amdgcn_s_setprio(1); _Pragma("unroll") for (int m = 0; m < 4; ++m) _Pragma("unroll") for (int n = 0; n < 2; ++n) _Pragma("unroll") for (int k = 0; k < 2; ++k) \
;         acc[ai][bj][m][n] = __builtin_amdgcn_mfma_f32_16x16x32_bf16(Bt[n][k], At[m][k], acc[ai][bj][m][n], 0, 0, 0); __builtin_amdgcn_s_setprio(0); } while (0)
; #define PG8_WAIT_V(n) asm volatile("s_waitcnt vmcnt(" #n ")" ::: "memory")
; #define PG8_WAIT_L(n) asm volatile("s_waitcnt lgkmcnt(" #n ")" ::: "memory")
; #define PG8_BAR __builtin_amdgcn_s_barrier()
; #define PG8_SCHED __builtin_amdgcn_sched_barrier(0)
; template <class Epi, class Sched, bool ALIGN_EPI>
; __device__ __forceinline__ void gemm_phase(LAS unsigned char* lds, const Gemm g, const Sched& S, const Epi& E) {
;     ...
;             const bool last = (t == nt - 2);
;             const unsigned kb1 = (unsigned)(t + 1) * 128u, kb2 = last ? 0u : (unsigned)(t + 2) * 128u;
;             if (last) { vc00 = vn00; vc01 = vn01; }
;             PG8_LDB(B0, 0, 0); PG8_LDB(B1, 0, 1); PG8_SCHED; PG8_LDA(At, 0, 0); PG8_STAGE_A(PG8_SA(1, 1), vc10, vc11, kb1);
;             PG8_WAIT_V(12); PG8_WAIT_L(0); PG8_BAR; PG8_MMA(0, 0, At, B0); PG8_MMA(0, 1, At, B1); PG8_BAR; PG8_SCHED;
.LBB0_2251:
	v_add_u32_e32 v162, 0x10000, v240
	v_add_u32_e32 v174, 0x14000, v240
	ds_read_b128 v[178:181], v162
	ds_read_b128 v[182:185], v162 offset:1024
	ds_read_b128 v[186:189], v162 offset:2048
	ds_read_b128 v[190:193], v162 offset:3072
	ds_read_b128 v[162:165], v174
	ds_read_b128 v[166:169], v174 offset:1024
	ds_read_b128 v[170:173], v174 offset:2048
	ds_read_b128 v[174:177], v174 offset:3072
	s_add_i32 s54, s53, 2
	s_add_i32 m0, s40, 0xc000
	s_add_u32 s4, s90, s22
	s_addc_u32 s5, s91, s23
	s_waitcnt lgkmcnt(0)
	ds_read_b128 v[194:197], v241
	ds_read_b128 v[198:201], v241 offset:1024
	ds_read_b128 v[202:205], v241 offset:2048
	ds_read_b128 v[206:209], v241 offset:3072
	ds_read_b128 v[210:213], v241 offset:4096
	ds_read_b128 v[214:217], v241 offset:5120
	ds_read_b128 v[218:221], v241 offset:6144
	ds_read_b128 v[222:225], v241 offset:7168
	global_load_lds_dwordx4 v234, s[4:5]
	s_add_i32 m0, s40, 0xe000
	s_nop 0
	global_load_lds_dwordx4 v235, s[4:5]
	s_waitcnt vmcnt(12)
	s_waitcnt lgkmcnt(0)
	s_barrier
	s_setprio 1
	s_waitcnt lgkmcnt(0)
	v_mfma_f32_16x16x32_bf16 v[158:161], v[178:181], v[194:197], v[158:161]
	v_mfma_f32_16x16x32_bf16 v[150:153], v[186:189], v[194:197], v[150:153]
	v_mfma_f32_16x16x32_bf16 v[142:145], v[178:181], v[202:205], v[142:145]
	v_mfma_f32_16x16x32_bf16 v[134:137], v[186:189], v[202:205], v[134:137]
	v_mfma_f32_16x16x32_bf16 v[126:129], v[178:181], v[210:213], v[126:129]
	v_mfma_f32_16x16x32_bf16 v[118:121], v[186:189], v[210:213], v[118:121]
	v_mfma_f32_16x16x32_bf16 v[110:113], v[178:181], v[218:221], v[110:113]
	v_mfma_f32_16x16x32_bf16 v[102:105], v[186:189], v[218:221], v[102:105]
	v_mfma_f32_16x16x32_bf16 v[158:161], v[182:185], v[198:201], v[158:161]
	v_mfma_f32_16x16x32_bf16 v[150:153], v[190:193], v[198:201], v[150:153]
	v_mfma_f32_16x16x32_bf16 v[142:145], v[182:185], v[206:209], v[142:145]
	v_mfma_f32_16x16x32_bf16 v[134:137], v[190:193], v[206:209], v[134:137]
	v_mfma_f32_16x16x32_bf16 v[126:129], v[182:185], v[214:217], v[126:129]
	v_mfma_f32_16x16x32_bf16 v[118:121], v[190:193], v[214:217], v[118:121]
	v_mfma_f32_16x16x32_bf16 v[110:113], v[182:185], v[222:225], v[110:113]
	v_mfma_f32_16x16x32_bf16 v[102:105], v[190:193], v[222:225], v[102:105]
	s_setprio 0
	s_setprio 1
	v_mfma_f32_16x16x32_bf16 v[154:157], v[162:165], v[194:197], v[154:157]
	v_mfma_f32_16x16x32_bf16 v[146:149], v[170:173], v[194:197], v[146:149]
	v_mfma_f32_16x16x32_bf16 v[138:141], v[162:165], v[202:205], v[138:141]
	v_mfma_f32_16x16x32_bf16 v[130:133], v[170:173], v[202:205], v[130:133]
	v_mfma_f32_16x16x32_bf16 v[122:125], v[162:165], v[210:213], v[122:125]
	v_mfma_f32_16x16x32_bf16 v[114:117], v[170:173], v[210:213], v[114:117]
	v_mfma_f32_16x16x32_bf16 v[106:109], v[162:165], v[218:221], v[106:109]
	v_mfma_f32_16x16x32_bf16 v[98:101], v[170:173], v[218:221], v[98:101]
	v_mfma_f32_16x16x32_bf16 v[154:157], v[166:169], v[198:201], v[154:157]
	v_mfma_f32_16x16x32_bf16 v[146:149], v[174:177], v[198:201], v[146:149]
	v_mfma_f32_16x16x32_bf16 v[138:141], v[166:169], v[206:209], v[138:141]
	v_mfma_f32_16x16x32_bf16 v[130:133], v[174:177], v[206:209], v[130:133]
	v_mfma_f32_16x16x32_bf16 v[122:125], v[166:169], v[214:217], v[122:125]
	v_mfma_f32_16x16x32_bf16 v[114:117], v[174:177], v[214:217], v[114:117]
	v_mfma_f32_16x16x32_bf16 v[106:109], v[166:169], v[222:225], v[106:109]
	v_mfma_f32_16x16x32_bf16 v[98:101], v[174:177], v[222:225], v[98:101]
	s_setprio 0
	s_barrier
	s_cmp_lt_u32 s54, 13
	s_mov_b64 s[6:7], -1
	s_cbranch_scc0 .LBB0_2253
	s_add_u32 s4, s20, 0x30000
	s_addc_u32 s5, s21, 0
	s_mov_b64 s[6:7], 0

; #define PG8_BWAIT(n) asm volatile("s_waitcnt vmcnt(" #n ")" : "+v"(bv[0]), "+v"(bv[1]), "+v"(bv[2]), "+v"(bv[3]), "+v"(bv[4]), "+v"(bv[5]), "+v"(bv[6]), "+v"(bv[7]) :: "memory")
; #define PG8_STAGE_A(bufoff, V0, V1, kb) do { \
;         __builtin_amdgcn_global_load_lds((const unsigned*)((Abase + (kb)) + (V0)), (LAS unsigned*)(lds + (bufoff) + ldsw), 16, 0, 0); \
;         __builtin_amdgcn_global_load_lds((const unsigned*)((Abase + (kb)) + (V1)), (LAS unsigned*)(lds + (bufoff) + ldsw + 8192), 16, 0, 0); } while (0)
; #define PG8_LDA(dst, b, h) do { _Pragma("unroll") for (int m = 0; m < 4; ++m) _Pragma("unroll") for (int k = 0; k < 2; ++k) dst[m][k] = *(const LAS bf16x8*)(lds + PG8_SA(b, h) + aoff + m * 2048 + k * 1024); } while (0)
; #define PG8_MMA(ai, bj, At, Bt) do { __builtin_amdgcn_s_setprio(1); _Pragma("unroll") for (int m = 0; m < 4; ++m) _Pragma("unroll") for (int n = 0; n < 2; ++n) _Pragma("unroll") for (int k = 0; k < 2; ++k) \
;         acc[ai][bj][m][n] = __builtin_amdgcn_mfma_f32_16x16x32_bf16(Bt[n][k], At[m][k], acc[ai][bj][m][n], 0, 0, 0); __builtin_amdgcn_s_setprio(0); } while (0)
; #define PG8_WAIT_V(n) asm volatile("s_waitcnt vmcnt(" #n ")" ::: "memory")
; #define PG8_WAIT_L(n) asm volatile("s_waitcnt lgkmcnt(" #n ")" ::: "memory")
; #define PG8_BAR __builtin_amdgcn_s_barrier()
; #define PG8_SCHED __builtin_amdgcn_sched_barrier(0)
; template <class Epi, class Sched, bool ALIGN_EPI>
; __device__ __forceinline__ void gemm_phase(LAS unsigned char* lds, const Gemm g, const Sched& S, const Epi& E) {
;     ...
;             PG8_BWAIT(2); PG8_BCOMMIT(0); PG8_SCHED; PG8_LDA(At, 0, 1); PG8_BISSUE(t + 3 >= nt ? pbn + (size_t)(t + 3 - nt) * 64 * Sched::LDN : pbc + (size_t)(t + 3) * 64 * Sched::LDN); PG8_STAGE_A(PG8_SA(0, 0), vc00, vc01, kb2);
;             PG8_WAIT_V(12); PG8_WAIT_L(0); PG8_BAR; if (half1) { PG8_MMA(1, 0, At, B0); PG8_MMA(1, 1, At, B1); } PG8_BAR; PG8_SCHED;
.LBB0_2255:
	s_add_i32 s2, s22, 0xe8940080
	s_cmp_eq_u32 s53, 12
	s_waitcnt vmcnt(2)
	s_nop 0
	v_cvt_pk_bf16_f32 v194, v2, v6
	v_cvt_pk_bf16_f32 v198, v3, v7
	v_cvt_pk_bf16_f32 v202, v4, v8
	v_cvt_pk_bf16_f32 v206, v5, v9
	global_load_dwordx4 v[2:5], v231, s[4:5] offset:0
	s_cselect_b64 s[6:7], -1, 0
	global_load_dwordx4 v[6:9], v231, s[4:5] offset:0x400
	v_cvt_pk_bf16_f32 v195, v10, v14
	v_cvt_pk_bf16_f32 v199, v11, v15
	v_cvt_pk_bf16_f32 v203, v12, v16
	v_cvt_pk_bf16_f32 v207, v13, v17
	s_and_b64 s[26:27], s[6:7], exec
	global_load_dwordx4 v[10:13], v231, s[4:5] offset:0x800
	s_cselect_b32 s2, 0, s2
	global_load_dwordx4 v[14:17], v231, s[4:5] offset:0xc00
	v_cvt_pk_bf16_f32 v196, v18, v22
	v_cvt_pk_bf16_f32 v200, v19, v23
	v_cvt_pk_bf16_f32 v204, v20, v24
	v_cvt_pk_bf16_f32 v208, v21, v25
	s_add_u32 s4, s4, 0x1000
	s_addc_u32 s5, s5, 0
	global_load_dwordx4 v[18:21], v231, s[4:5] offset:0
	global_load_dwordx4 v[22:25], v231, s[4:5] offset:0x400
	v_cvt_pk_bf16_f32 v197, v26, v30
	v_cvt_pk_bf16_f32 v201, v27, v31
	v_cvt_pk_bf16_f32 v205, v28, v32
	v_cvt_pk_bf16_f32 v209, v29, v33
	global_load_dwordx4 v[26:29], v231, s[4:5] offset:0x800
	global_load_dwordx4 v[30:33], v231, s[4:5] offset:0xc00
	v_add_u32_e32 v210, 0x10000, v232
	v_xor_b32_e32 v211, 64, v210
	v_xor_b32_e32 v212, 0x80, v210
	v_xor_b32_e32 v213, 0xc0, v210
	ds_write_b128 v210, v[194:197]
	ds_write_b128 v211, v[198:201]
	ds_write_b128 v212, v[202:205]
	ds_write_b128 v213, v[206:209]
	ds_read_b128 v[218:221], v241 offset:16384
	ds_read_b128 v[222:225], v241 offset:17408
	ds_read_b128 v[210:213], v241 offset:18432
	ds_read_b128 v[214:217], v241 offset:19456
	ds_read_b128 v[202:205], v241 offset:20480
	ds_read_b128 v[206:209], v241 offset:21504
	ds_read_b128 v[194:197], v241 offset:22528
	ds_read_b128 v[198:201], v241 offset:23552
	v_readlane_b32 s4, v255, 13
	v_readlane_b32 s5, v255, 14
	s_add_u32 s26, s4, s2
	s_mov_b32 m0, s40
	v_cndmask_b32_e64 v226, v226, v242, s[6:7]
	s_addc_u32 s27, s5, 0
	v_cndmask_b32_e64 v228, v228, v243, s[6:7]
	global_load_lds_dwordx4 v226, s[26:27]
	s_mov_b32 m0, s41
	v_cndmask_b32_e64 v229, 0, 1, s[24:25]
	global_load_lds_dwordx4 v228, s[26:27]
	s_waitcnt vmcnt(12)
	s_waitcnt lgkmcnt(0)
	v_cmp_ne_u32_e64 s[4:5], 1, v229
	s_andn2_b64 vcc, exec, s[24:25]
	s_barrier
	s_cbranch_vccnz .LBB0_2257
	s_setprio 1
	s_waitcnt lgkmcnt(0)
	v_mfma_f32_16x16x32_bf16 v[94:97], v[178:181], v[218:221], v[94:97]
	v_mfma_f32_16x16x32_bf16 v[86:89], v[186:189], v[218:221], v[86:89]
	v_mfma_f32_16x16x32_bf16 v[78:81], v[178:181], v[210:213], v[78:81]
	v_mfma_f32_16x16x32_bf16 v[70:73], v[186:189], v[210:213], v[70:73]
	v_mfma_f32_16x16x32_bf16 v[62:65], v[178:181], v[202:205], v[62:65]
	v_mfma_f32_16x16x32_bf16 v[54:57], v[186:189], v[202:205], v[54:57]
	v_mfma_f32_16x16x32_bf16 v[46:49], v[178:181], v[194:197], v[46:49]
	v_mfma_f32_16x16x32_bf16 v[38:41], v[186:189], v[194:197], v[38:41]
	v_mfma_f32_16x16x32_bf16 v[94:97], v[182:185], v[222:225], v[94:97]
	v_mfma_f32_16x16x32_bf16 v[86:89], v[190:193], v[222:225], v[86:89]
	v_mfma_f32_16x16x32_bf16 v[78:81], v[182:185], v[214:217], v[78:81]
	v_mfma_f32_16x16x32_bf16 v[70:73], v[190:193], v[214:217], v[70:73]
	v_mfma_f32_16x16x32_bf16 v[62:65], v[182:185], v[206:209], v[62:65]
	v_mfma_f32_16x16x32_bf16 v[54:57], v[190:193], v[206:209], v[54:57]
	v_mfma_f32_16x16x32_bf16 v[46:49], v[182:185], v[198:201], v[46:49]
	v_mfma_f32_16x16x32_bf16 v[38:41], v[190:193], v[198:201], v[38:41]
	s_setprio 0
	s_setprio 1
	v_mfma_f32_16x16x32_bf16 v[90:93], v[162:165], v[218:221], v[90:93]
	v_mfma_f32_16x16x32_bf16 v[82:85], v[170:173], v[218:221], v[82:85]
	v_mfma_f32_16x16x32_bf16 v[74:77], v[162:165], v[210:213], v[74:77]
	v_mfma_f32_16x16x32_bf16 v[66:69], v[170:173], v[210:213], v[66:69]
	v_mfma_f32_16x16x32_bf16 v[58:61], v[162:165], v[202:205], v[58:61]
	v_mfma_f32_16x16x32_bf16 v[50:53], v[170:173], v[202:205], v[50:53]
	v_mfma_f32_16x16x32_bf16 v[42:45], v[162:165], v[194:197], v[42:45]
	v_mfma_f32_16x16x32_bf16 v[34:37], v[170:173], v[194:197], v[34:37]
	v_mfma_f32_16x16x32_bf16 v[90:93], v[166:169], v[222:225], v[90:93]
	v_mfma_f32_16x16x32_bf16 v[82:85], v[174:177], v[222:225], v[82:85]
	v_mfma_f32_16x16x32_bf16 v[74:77], v[166:169], v[214:217], v[74:77]
	v_mfma_f32_16x16x32_bf16 v[66:69], v[174:177], v[214:217], v[66:69]
	v_mfma_f32_16x16x32_bf16 v[58:61], v[166:169], v[206:209], v[58:61]
	v_mfma_f32_16x16x32_bf16 v[50:53], v[174:177], v[206:209], v[50:53]
	v_mfma_f32_16x16x32_bf16 v[42:45], v[166:169], v[198:201], v[42:45]
	v_mfma_f32_16x16x32_bf16 v[34:37], v[174:177], v[198:201], v[34:37]
	s_setprio 0
; #define PG8_STAGE_A(bufoff, V0, V1, kb) do { \
;         __builtin_amdgcn_global_load_lds((const unsigned*)((Abase + (kb)) + (V0)), (LAS unsigned*)(lds + (bufoff) + ldsw), 16, 0, 0); \
;         __builtin_amdgcn_global_load_lds((const unsigned*)((Abase + (kb)) + (V1)), (LAS unsigned*)(lds + (bufoff) + ldsw + 8192), 16, 0, 0); } while (0)
; #define PG8_LDA(dst, b, h) do { _Pragma("unroll") for (int m = 0; m < 4; ++m) _Pragma("unroll") for (int k = 0; k < 2; ++k) dst[m][k] = *(const LAS bf16x8*)(lds + PG8_SA(b, h) + aoff + m * 2048 + k * 1024); } while (0)
; #define PG8_LDB(dst, b, h) do { _Pragma("unroll") for (int n = 0; n < 2; ++n) _Pragma("unroll") for (int k = 0; k < 2; ++k) dst[n][k] = *(const LAS bf16x8*)(lds + PG8_SB(b, h) + boff + n * 2048 + k * 1024); } while (0)
; #define PG8_MMA(ai, bj, At, Bt) do { __builtin_amdgcn_s_setprio(1); _Pragma("unroll") for (int m = 0; m < 4; ++m) _Pragma("unroll") for (int n = 0; n < 2; ++n) _Pragma("unroll") for (int k = 0; k < 2; ++k) \
;         acc[ai][bj][m][n] = __builtin_amdgcn_mfma_f32_16x16x32_bf16(Bt[n][k], At[m][k], acc[ai][bj][m][n], 0, 0, 0); __builtin_amdgcn_s_setprio(0); } while (0)
; #define PG8_WAIT_V(n) asm volatile("s_waitcnt vmcnt(" #n ")" ::: "memory")
; #define PG8_WAIT_L(n) asm volatile("s_waitcnt lgkmcnt(" #n ")" ::: "memory")
; #define PG8_BAR __builtin_amdgcn_s_barrier()
; #define PG8_SCHED __builtin_amdgcn_sched_barrier(0)
; template <class Epi, class Sched, bool ALIGN_EPI>
; __device__ __forceinline__ void gemm_phase(LAS unsigned char* lds, const Gemm g, const Sched& S, const Epi& E) {
;     ...
;             PG8_LDB(B0, 1, 0); PG8_LDB(B1, 1, 1); PG8_SCHED; PG8_LDA(At, 1, 0); PG8_STAGE_A(PG8_SA(0, 1), vc10, vc11, kb2);
;             PG8_WAIT_V(12); PG8_WAIT_L(0); PG8_BAR; PG8_MMA(0, 0, At, B0); PG8_MMA(0, 1, At, B1); PG8_BAR; PG8_SCHED;
.LBB0_2257:
	v_cndmask_b32_e64 v235, v235, v245, s[6:7]
	v_cndmask_b32_e64 v234, v234, v244, s[6:7]
	s_barrier
	v_add_u32_e32 v162, 0x18000, v240
	v_add_u32_e32 v174, 0x1c000, v240
	ds_read_b128 v[178:181], v162
	ds_read_b128 v[182:185], v162 offset:1024
	ds_read_b128 v[186:189], v162 offset:2048
	ds_read_b128 v[190:193], v162 offset:3072
	ds_read_b128 v[162:165], v174
	ds_read_b128 v[166:169], v174 offset:1024
	ds_read_b128 v[170:173], v174 offset:2048
	ds_read_b128 v[174:177], v174 offset:3072
	s_mov_b32 m0, s42
	s_waitcnt lgkmcnt(0)
	ds_read_b128 v[194:197], v241 offset:32768
	ds_read_b128 v[198:201], v241 offset:33792
	ds_read_b128 v[202:205], v241 offset:34816
	ds_read_b128 v[206:209], v241 offset:35840
	ds_read_b128 v[210:213], v241 offset:36864
	ds_read_b128 v[214:217], v241 offset:37888
	ds_read_b128 v[218:221], v241 offset:38912
	ds_read_b128 v[222:225], v241 offset:39936
	global_load_lds_dwordx4 v234, s[26:27]
	s_mov_b32 m0, s43
	s_nop 0
	global_load_lds_dwordx4 v235, s[26:27]
	s_waitcnt vmcnt(12)
	s_waitcnt lgkmcnt(0)
	s_barrier
	s_setprio 1
	s_waitcnt lgkmcnt(0)
	v_mfma_f32_16x16x32_bf16 v[158:161], v[178:181], v[194:197], v[158:161]
	v_mfma_f32_16x16x32_bf16 v[150:153], v[186:189], v[194:197], v[150:153]
	v_mfma_f32_16x16x32_bf16 v[142:145], v[178:181], v[202:205], v[142:145]
	v_mfma_f32_16x16x32_bf16 v[134:137], v[186:189], v[202:205], v[134:137]
	v_mfma_f32_16x16x32_bf16 v[126:129], v[178:181], v[210:213], v[126:129]
	v_mfma_f32_16x16x32_bf16 v[118:121], v[186:189], v[210:213], v[118:121]
	v_mfma_f32_16x16x32_bf16 v[110:113], v[178:181], v[218:221], v[110:113]
	v_mfma_f32_16x16x32_bf16 v[102:105], v[186:189], v[218:221], v[102:105]
	v_mfma_f32_16x16x32_bf16 v[158:161], v[182:185], v[198:201], v[158:161]
	v_mfma_f32_16x16x32_bf16 v[150:153], v[190:193], v[198:201], v[150:153]
	v_mfma_f32_16x16x32_bf16 v[142:145], v[182:185], v[206:209], v[142:145]
	v_mfma_f32_16x16x32_bf16 v[134:137], v[190:193], v[206:209], v[134:137]
	v_mfma_f32_16x16x32_bf16 v[126:129], v[182:185], v[214:217], v[126:129]
	v_mfma_f32_16x16x32_bf16 v[118:121], v[190:193], v[214:217], v[118:121]
	v_mfma_f32_16x16x32_bf16 v[110:113], v[182:185], v[222:225], v[110:113]
	v_mfma_f32_16x16x32_bf16 v[102:105], v[190:193], v[222:225], v[102:105]
	s_setprio 0
	s_setprio 1
	v_mfma_f32_16x16x32_bf16 v[154:157], v[162:165], v[194:197], v[154:157]
	v_mfma_f32_16x16x32_bf16 v[146:149], v[170:173], v[194:197], v[146:149]
	v_mfma_f32_16x16x32_bf16 v[138:141], v[162:165], v[202:205], v[138:141]
	v_mfma_f32_16x16x32_bf16 v[130:133], v[170:173], v[202:205], v[130:133]
	v_mfma_f32_16x16x32_bf16 v[122:125], v[162:165], v[210:213], v[122:125]
	v_mfma_f32_16x16x32_bf16 v[114:117], v[170:173], v[210:213], v[114:117]
	v_mfma_f32_16x16x32_bf16 v[106:109], v[162:165], v[218:221], v[106:109]
	v_mfma_f32_16x16x32_bf16 v[98:101], v[170:173], v[218:221], v[98:101]
	v_mfma_f32_16x16x32_bf16 v[154:157], v[166:169], v[198:201], v[154:157]
	v_mfma_f32_16x16x32_bf16 v[146:149], v[174:177], v[198:201], v[146:149]
	v_mfma_f32_16x16x32_bf16 v[138:141], v[166:169], v[206:209], v[138:141]
	v_mfma_f32_16x16x32_bf16 v[130:133], v[174:177], v[206:209], v[130:133]
	v_mfma_f32_16x16x32_bf16 v[122:125], v[166:169], v[214:217], v[122:125]
	v_mfma_f32_16x16x32_bf16 v[114:117], v[174:177], v[214:217], v[114:117]
	v_mfma_f32_16x16x32_bf16 v[106:109], v[166:169], v[222:225], v[106:109]
	v_mfma_f32_16x16x32_bf16 v[98:101], v[174:177], v[222:225], v[98:101]
	s_setprio 0
	s_barrier
	s_cmp_lt_u32 s54, 12
	s_mov_b64 s[28:29], -1
	s_cbranch_scc0 .LBB0_2259
	s_add_u32 s6, s20, 0x40000
	s_addc_u32 s7, s21, 0
	s_mov_b64 s[28:29], 0

; #define PG8_BWAIT(n) asm volatile("s_waitcnt vmcnt(" #n ")" : "+v"(bv[0]), "+v"(bv[1]), "+v"(bv[2]), "+v"(bv[3]), "+v"(bv[4]), "+v"(bv[5]), "+v"(bv[6]), "+v"(bv[7]) :: "memory")
; #define PG8_STAGE_A(bufoff, V0, V1, kb) do { \
;         __builtin_amdgcn_global_load_lds((const unsigned*)((Abase + (kb)) + (V0)), (LAS unsigned*)(lds + (bufoff) + ldsw), 16, 0, 0); \
;         __builtin_amdgcn_global_load_lds((const unsigned*)((Abase + (kb)) + (V1)), (LAS unsigned*)(lds + (bufoff) + ldsw + 8192), 16, 0, 0); } while (0)
; #define PG8_LDA(dst, b, h) do { _Pragma("unroll") for (int m = 0; m < 4; ++m) _Pragma("unroll") for (int k = 0; k < 2; ++k) dst[m][k] = *(const LAS bf16x8*)(lds + PG8_SA(b, h) + aoff + m * 2048 + k * 1024); } while (0)
; #define PG8_MMA(ai, bj, At, Bt) do { __builtin_amdgcn_s_setprio(1); _Pragma("unroll") for (int m = 0; m < 4; ++m) _Pragma("unroll") for (int n = 0; n < 2; ++n) _Pragma("unroll") for (int k = 0; k < 2; ++k) \
;         acc[ai][bj][m][n] = __builtin_amdgcn_mfma_f32_16x16x32_bf16(Bt[n][k], At[m][k], acc[ai][bj][m][n], 0, 0, 0); __builtin_amdgcn_s_setprio(0); } while (0)
; #define PG8_WAIT_V(n) asm volatile("s_waitcnt vmcnt(" #n ")" ::: "memory")
; #define PG8_WAIT_L(n) asm volatile("s_waitcnt lgkmcnt(" #n ")" ::: "memory")
; #define PG8_BAR __builtin_amdgcn_s_barrier()
; #define PG8_SCHED __builtin_amdgcn_sched_barrier(0)
; template <class Epi, class Sched, bool ALIGN_EPI>
; __device__ __forceinline__ void gemm_phase(LAS unsigned char* lds, const Gemm g, const Sched& S, const Epi& E) {
;     ...
;             PG8_BWAIT(2); PG8_BCOMMIT(1); PG8_SCHED; PG8_LDA(At, 1, 1); PG8_BISSUE(t + 4 >= nt ? pbn + (size_t)(t + 4 - nt) * 64 * Sched::LDN : pbc + (size_t)(t + 4) * 64 * Sched::LDN); PG8_STAGE_A(PG8_SA(1, 0), vc00, vc01, kb2 + 128u);
;             PG8_WAIT_V(12); PG8_WAIT_L(0); PG8_BAR; if (half1) { PG8_MMA(1, 0, At, B0); PG8_MMA(1, 1, At, B1); } PG8_BAR; PG8_SCHED;
.LBB0_2261:
	s_waitcnt vmcnt(2)
	s_nop 0
	v_cvt_pk_bf16_f32 v194, v2, v6
	v_cvt_pk_bf16_f32 v198, v3, v7
	v_cvt_pk_bf16_f32 v202, v4, v8
	v_cvt_pk_bf16_f32 v206, v5, v9
	global_load_dwordx4 v[2:5], v231, s[6:7] offset:0
	global_load_dwordx4 v[6:9], v231, s[6:7] offset:0x400
	v_cvt_pk_bf16_f32 v195, v10, v14
	v_cvt_pk_bf16_f32 v199, v11, v15
	v_cvt_pk_bf16_f32 v203, v12, v16
	v_cvt_pk_bf16_f32 v207, v13, v17
	global_load_dwordx4 v[10:13], v231, s[6:7] offset:0x800
	global_load_dwordx4 v[14:17], v231, s[6:7] offset:0xc00
	v_cvt_pk_bf16_f32 v196, v18, v22
	v_cvt_pk_bf16_f32 v200, v19, v23
	v_cvt_pk_bf16_f32 v204, v20, v24
	v_cvt_pk_bf16_f32 v208, v21, v25
	s_add_u32 s6, s6, 0x1000
	s_addc_u32 s7, s7, 0
	global_load_dwordx4 v[18:21], v231, s[6:7] offset:0
	global_load_dwordx4 v[22:25], v231, s[6:7] offset:0x400
	v_cvt_pk_bf16_f32 v197, v26, v30
	v_cvt_pk_bf16_f32 v201, v27, v31
	v_cvt_pk_bf16_f32 v205, v28, v32
	v_cvt_pk_bf16_f32 v209, v29, v33
	v_lshl_add_u64 v[246:247], s[26:27], 0, v[226:227]
	v_mov_b32_e32 v229, v227
	global_load_dwordx4 v[26:29], v231, s[6:7] offset:0x800
	s_mov_b32 m0, s44
	v_lshl_add_u64 v[248:249], s[26:27], 0, v[228:229]
	global_load_dwordx4 v[30:33], v231, s[6:7] offset:0xc00
	v_add_u32_e32 v210, 0x18000, v232
	v_xor_b32_e32 v211, 64, v210
	v_xor_b32_e32 v212, 0x80, v210
	v_xor_b32_e32 v213, 0xc0, v210
	ds_write_b128 v210, v[194:197]
	ds_write_b128 v211, v[198:201]
	ds_write_b128 v212, v[202:205]
	ds_write_b128 v213, v[206:209]
	ds_read_b128 v[218:221], v241 offset:49152
	ds_read_b128 v[222:225], v241 offset:50176
	ds_read_b128 v[210:213], v241 offset:51200
	ds_read_b128 v[214:217], v241 offset:52224
	ds_read_b128 v[202:205], v241 offset:53248
	ds_read_b128 v[206:209], v241 offset:54272
	ds_read_b128 v[194:197], v241 offset:55296
	ds_read_b128 v[198:201], v241 offset:56320
	v_lshl_add_u64 v[246:247], v[246:247], 0, s[12:13]
	global_load_lds_dwordx4 v[246:247], off
	v_lshl_add_u64 v[246:247], v[248:249], 0, s[12:13]
	s_mov_b32 m0, s45
	s_and_b64 vcc, exec, s[4:5]
	global_load_lds_dwordx4 v[246:247], off
	s_waitcnt vmcnt(12)
	s_waitcnt lgkmcnt(0)
	s_barrier
	s_cbranch_vccnz .LBB0_2263
	s_setprio 1
	s_waitcnt lgkmcnt(0)
	v_mfma_f32_16x16x32_bf16 v[94:97], v[178:181], v[218:221], v[94:97]
	v_mfma_f32_16x16x32_bf16 v[86:89], v[186:189], v[218:221], v[86:89]
	v_mfma_f32_16x16x32_bf16 v[78:81], v[178:181], v[210:213], v[78:81]
	v_mfma_f32_16x16x32_bf16 v[70:73], v[186:189], v[210:213], v[70:73]
	v_mfma_f32_16x16x32_bf16 v[62:65], v[178:181], v[202:205], v[62:65]
	v_mfma_f32_16x16x32_bf16 v[54:57], v[186:189], v[202:205], v[54:57]
	v_mfma_f32_16x16x32_bf16 v[46:49], v[178:181], v[194:197], v[46:49]
	v_mfma_f32_16x16x32_bf16 v[38:41], v[186:189], v[194:197], v[38:41]
	v_mfma_f32_16x16x32_bf16 v[94:97], v[182:185], v[222:225], v[94:97]
	v_mfma_f32_16x16x32_bf16 v[86:89], v[190:193], v[222:225], v[86:89]
	v_mfma_f32_16x16x32_bf16 v[78:81], v[182:185], v[214:217], v[78:81]
	v_mfma_f32_16x16x32_bf16 v[70:73], v[190:193], v[214:217], v[70:73]
	v_mfma_f32_16x16x32_bf16 v[62:65], v[182:185], v[206:209], v[62:65]
	v_mfma_f32_16x16x32_bf16 v[54:57], v[190:193], v[206:209], v[54:57]
	v_mfma_f32_16x16x32_bf16 v[46:49], v[182:185], v[198:201], v[46:49]
	v_mfma_f32_16x16x32_bf16 v[38:41], v[190:193], v[198:201], v[38:41]
	s_setprio 0
	s_setprio 1
	v_mfma_f32_16x16x32_bf16 v[90:93], v[162:165], v[218:221], v[90:93]
	v_mfma_f32_16x16x32_bf16 v[82:85], v[170:173], v[218:221], v[82:85]
	v_mfma_f32_16x16x32_bf16 v[74:77], v[162:165], v[210:213], v[74:77]
	v_mfma_f32_16x16x32_bf16 v[66:69], v[170:173], v[210:213], v[66:69]
	v_mfma_f32_16x16x32_bf16 v[58:61], v[162:165], v[202:205], v[58:61]
	v_mfma_f32_16x16x32_bf16 v[50:53], v[170:173], v[202:205], v[50:53]
	v_mfma_f32_16x16x32_bf16 v[42:45], v[162:165], v[194:197], v[42:45]
	v_mfma_f32_16x16x32_bf16 v[34:37], v[170:173], v[194:197], v[34:37]
	v_mfma_f32_16x16x32_bf16 v[90:93], v[166:169], v[222:225], v[90:93]
	v_mfma_f32_16x16x32_bf16 v[82:85], v[174:177], v[222:225], v[82:85]
	v_mfma_f32_16x16x32_bf16 v[74:77], v[166:169], v[214:217], v[74:77]
	v_mfma_f32_16x16x32_bf16 v[66:69], v[174:177], v[214:217], v[66:69]
	v_mfma_f32_16x16x32_bf16 v[58:61], v[166:169], v[206:209], v[58:61]
	v_mfma_f32_16x16x32_bf16 v[50:53], v[174:177], v[206:209], v[50:53]
	v_mfma_f32_16x16x32_bf16 v[42:45], v[166:169], v[198:201], v[42:45]
	v_mfma_f32_16x16x32_bf16 v[34:37], v[174:177], v[198:201], v[34:37]
	s_setprio 0

; #define PG8_BWAIT(n) asm volatile("s_waitcnt vmcnt(" #n ")" : "+v"(bv[0]), "+v"(bv[1]), "+v"(bv[2]), "+v"(bv[3]), "+v"(bv[4]), "+v"(bv[5]), "+v"(bv[6]), "+v"(bv[7]) :: "memory")
; #define PG8_STAGE_A(bufoff, V0, V1, kb) do { \
;         __builtin_amdgcn_global_load_lds((const unsigned*)((Abase + (kb)) + (V0)), (LAS unsigned*)(lds + (bufoff) + ldsw), 16, 0, 0); \
;         __builtin_amdgcn_global_load_lds((const unsigned*)((Abase + (kb)) + (V1)), (LAS unsigned*)(lds + (bufoff) + ldsw + 8192), 16, 0, 0); } while (0)
; #define PG8_LDA(dst, b, h) do { _Pragma("unroll") for (int m = 0; m < 4; ++m) _Pragma("unroll") for (int k = 0; k < 2; ++k) dst[m][k] = *(const LAS bf16x8*)(lds + PG8_SA(b, h) + aoff + m * 2048 + k * 1024); } while (0)
; #define PG8_LDB(dst, b, h) do { _Pragma("unroll") for (int n = 0; n < 2; ++n) _Pragma("unroll") for (int k = 0; k < 2; ++k) dst[n][k] = *(const LAS bf16x8*)(lds + PG8_SB(b, h) + boff + n * 2048 + k * 1024); } while (0)
; #define PG8_MMA(ai, bj, At, Bt) do { __builtin_amdgcn_s_setprio(1); _Pragma("unroll") for (int m = 0; m < 4; ++m) _Pragma("unroll") for (int n = 0; n < 2; ++n) _Pragma("unroll") for (int k = 0; k < 2; ++k) \
;         acc[ai][bj][m][n] = __builtin_amdgcn_mfma_f32_16x16x32_bf16(Bt[n][k], At[m][k], acc[ai][bj][m][n], 0, 0, 0); __builtin_amdgcn_s_setprio(0); } while (0)
; #define PG8_WAIT_V(n) asm volatile("s_waitcnt vmcnt(" #n ")" ::: "memory")
; #define PG8_WAIT_L(n) asm volatile("s_waitcnt lgkmcnt(" #n ")" ::: "memory")
; #define PG8_BAR __builtin_amdgcn_s_barrier()
; template <class Epi, class Sched, bool ALIGN_EPI>
; __device__ __forceinline__ void gemm_phase(LAS unsigned char* lds, const Gemm g, const Sched& S, const Epi& E) {
;     ...
;             PG8_LDB(B0, 0, 0); PG8_LDB(B1, 0, 1); PG8_SCHED; PG8_LDA(At, 0, 0); PG8_STAGE_A(PG8_SA(1, 1), vc10, vc11, kb1);
;             PG8_WAIT_V(12); PG8_WAIT_L(0); PG8_BAR; PG8_MMA(0, 0, At, B0); PG8_MMA(0, 1, At, B1); PG8_BAR; PG8_SCHED;
;             if (last) { vc10 = vn10; vc11 = vn11; }
;             PG8_BWAIT(2); PG8_BCOMMIT(0); PG8_SCHED; PG8_LDA(At, 0, 1); PG8_BISSUE(t + 3 >= nt ? pbn + (size_t)(t + 3 - nt) * 64 * Sched::LDN : pbc + (size_t)(t + 3) * 64 * Sched::LDN); PG8_STAGE_A(PG8_SA(0, 0), vc00, vc01, kb2);
;             PG8_WAIT_V(12); PG8_WAIT_L(0); PG8_BAR; if (half1) { PG8_MMA(1, 0, At, B0); PG8_MMA(1, 1, At, B1); } PG8_BAR; PG8_SCHED;
.LBB0_2448:
	v_add_u32_e32 v162, 0x10000, v247
	v_add_u32_e32 v174, 0x14000, v247
	ds_read_b128 v[178:181], v162
	ds_read_b128 v[182:185], v162 offset:1024
	ds_read_b128 v[186:189], v162 offset:2048
	ds_read_b128 v[190:193], v162 offset:3072
	ds_read_b128 v[162:165], v174
	ds_read_b128 v[166:169], v174 offset:1024
	ds_read_b128 v[170:173], v174 offset:2048
	ds_read_b128 v[174:177], v174 offset:3072
	s_lshl_b32 s5, s50, 7
	s_add_i32 s4, s5, 0x100
	v_cndmask_b32_e64 v228, v228, v250, s[28:29]
	v_readlane_b32 s54, v254, 53
	v_readlane_b32 s55, v254, 54
	s_add_u32 s30, s54, s5
	s_addc_u32 s31, s55, 0
	v_lshl_add_u64 v[236:237], s[30:31], 0, v[230:231]
	v_lshl_add_u64 v[236:237], v[236:237], 0, s[16:17]
	s_add_i32 m0, s35, 0xc000
	v_mov_b32_e32 v233, v231
	s_waitcnt lgkmcnt(0)
	ds_read_b128 v[194:197], v248
	ds_read_b128 v[198:201], v248 offset:1024
	ds_read_b128 v[202:205], v248 offset:2048
	ds_read_b128 v[206:209], v248 offset:3072
	ds_read_b128 v[210:213], v248 offset:4096
	ds_read_b128 v[214:217], v248 offset:5120
	ds_read_b128 v[218:221], v248 offset:6144
	ds_read_b128 v[222:225], v248 offset:7168
	global_load_lds_dwordx4 v[236:237], off
	v_lshl_add_u64 v[236:237], s[30:31], 0, v[232:233]
	v_lshl_add_u64 v[236:237], v[236:237], 0, s[16:17]
	s_add_i32 m0, s35, 0xe000
	s_nop 0
	global_load_lds_dwordx4 v[236:237], off
	s_waitcnt vmcnt(12)
	s_waitcnt lgkmcnt(0)
	s_barrier
	s_setprio 1
	s_waitcnt lgkmcnt(0)
	v_mfma_f32_16x16x32_bf16 v[158:161], v[178:181], v[194:197], v[158:161]
	v_mfma_f32_16x16x32_bf16 v[154:157], v[186:189], v[194:197], v[154:157]
	v_mfma_f32_16x16x32_bf16 v[142:145], v[178:181], v[202:205], v[142:145]
	v_mfma_f32_16x16x32_bf16 v[138:141], v[186:189], v[202:205], v[138:141]
	v_mfma_f32_16x16x32_bf16 v[126:129], v[178:181], v[210:213], v[126:129]
	v_mfma_f32_16x16x32_bf16 v[122:125], v[186:189], v[210:213], v[122:125]
	v_mfma_f32_16x16x32_bf16 v[110:113], v[178:181], v[218:221], v[110:113]
	v_mfma_f32_16x16x32_bf16 v[106:109], v[186:189], v[218:221], v[106:109]
	v_mfma_f32_16x16x32_bf16 v[158:161], v[182:185], v[198:201], v[158:161]
	v_mfma_f32_16x16x32_bf16 v[154:157], v[190:193], v[198:201], v[154:157]
	v_mfma_f32_16x16x32_bf16 v[142:145], v[182:185], v[206:209], v[142:145]
	v_mfma_f32_16x16x32_bf16 v[138:141], v[190:193], v[206:209], v[138:141]
	v_mfma_f32_16x16x32_bf16 v[126:129], v[182:185], v[214:217], v[126:129]
	v_mfma_f32_16x16x32_bf16 v[122:125], v[190:193], v[214:217], v[122:125]
	v_mfma_f32_16x16x32_bf16 v[110:113], v[182:185], v[222:225], v[110:113]
	v_mfma_f32_16x16x32_bf16 v[106:109], v[190:193], v[222:225], v[106:109]
	s_setprio 0
	s_setprio 1
	v_mfma_f32_16x16x32_bf16 v[150:153], v[162:165], v[194:197], v[150:153]
	v_mfma_f32_16x16x32_bf16 v[146:149], v[170:173], v[194:197], v[146:149]
	v_mfma_f32_16x16x32_bf16 v[134:137], v[162:165], v[202:205], v[134:137]
	v_mfma_f32_16x16x32_bf16 v[130:133], v[170:173], v[202:205], v[130:133]
	v_mfma_f32_16x16x32_bf16 v[118:121], v[162:165], v[210:213], v[118:121]
	v_mfma_f32_16x16x32_bf16 v[114:117], v[170:173], v[210:213], v[114:117]
	v_mfma_f32_16x16x32_bf16 v[102:105], v[162:165], v[218:221], v[102:105]
	v_mfma_f32_16x16x32_bf16 v[98:101], v[170:173], v[218:221], v[98:101]
	v_mfma_f32_16x16x32_bf16 v[150:153], v[166:169], v[198:201], v[150:153]
	v_mfma_f32_16x16x32_bf16 v[146:149], v[174:177], v[198:201], v[146:149]
	v_mfma_f32_16x16x32_bf16 v[134:137], v[166:169], v[206:209], v[134:137]
	v_mfma_f32_16x16x32_bf16 v[130:133], v[174:177], v[206:209], v[130:133]
	v_mfma_f32_16x16x32_bf16 v[118:121], v[166:169], v[214:217], v[118:121]
	v_mfma_f32_16x16x32_bf16 v[114:117], v[174:177], v[214:217], v[114:117]
	v_mfma_f32_16x16x32_bf16 v[102:105], v[166:169], v[222:225], v[102:105]
	v_mfma_f32_16x16x32_bf16 v[98:101], v[174:177], v[222:225], v[98:101]
	s_setprio 0
	s_barrier
	s_add_i32 s10, s50, -1
	s_lshl_b64 s[30:31], s[10:11], 18
	s_add_u32 s5, s47, s30
	s_addc_u32 s10, s21, s31
	s_and_b64 s[30:31], s[26:27], exec
	s_cselect_b32 s30, s48, s5
	s_cselect_b32 s31, s49, s10
	s_add_u32 s52, s30, 0x1000
	s_waitcnt vmcnt(2)
	v_cndmask_b32_e64 v226, v226, v249, s[28:29]
	v_cvt_pk_bf16_f32 v194, v2, v6
	v_cvt_pk_bf16_f32 v198, v3, v7
	v_cvt_pk_bf16_f32 v202, v4, v8
	v_cvt_pk_bf16_f32 v206, v5, v9
	global_load_dwordx4 v[2:5], v240, s[30:31] offset:0
	s_addc_u32 s53, s31, 0
	global_load_dwordx4 v[6:9], v240, s[52:53] offset:0
	v_cvt_pk_bf16_f32 v195, v10, v14
	v_cvt_pk_bf16_f32 v199, v11, v15
	v_cvt_pk_bf16_f32 v203, v12, v16
	v_cvt_pk_bf16_f32 v207, v13, v17
	s_add_u32 s52, s30, 0x2000
	s_addc_u32 s53, s31, 0
	global_load_dwordx4 v[10:13], v240, s[52:53] offset:0
	s_add_u32 s52, s30, 0x3000
	s_addc_u32 s53, s31, 0
	global_load_dwordx4 v[14:17], v240, s[52:53] offset:0
	v_cvt_pk_bf16_f32 v196, v18, v22
	v_cvt_pk_bf16_f32 v200, v19, v23
	v_cvt_pk_bf16_f32 v204, v20, v24
	v_cvt_pk_bf16_f32 v208, v21, v25
	s_add_u32 s52, s30, 0x4000
	s_addc_u32 s53, s31, 0
	global_load_dwordx4 v[18:21], v240, s[52:53] offset:0
	s_add_u32 s52, s30, 0x5000
	s_addc_u32 s53, s31, 0
	global_load_dwordx4 v[22:25], v240, s[52:53] offset:0
	v_cvt_pk_bf16_f32 v197, v26, v30
	v_cvt_pk_bf16_f32 v201, v27, v31
	v_cvt_pk_bf16_f32 v205, v28, v32
	v_cvt_pk_bf16_f32 v209, v29, v33
	s_add_u32 s52, s30, 0x6000
	s_addc_u32 s53, s31, 0
	s_add_u32 s30, s30, 0x7000
	global_load_dwordx4 v[26:29], v240, s[52:53] offset:0
	s_addc_u32 s31, s31, 0
	global_load_dwordx4 v[30:33], v240, s[30:31] offset:0
	v_add_u32_e32 v210, 0x10000, v242
	v_xor_b32_e32 v211, 64, v210
	v_xor_b32_e32 v212, 0x80, v210
	v_xor_b32_e32 v213, 0xc0, v210
	ds_write_b128 v210, v[194:197]
	ds_write_b128 v211, v[198:201]
	ds_write_b128 v212, v[202:205]
	ds_write_b128 v213, v[206:209]
	ds_read_b128 v[218:221], v248 offset:16384
	ds_read_b128 v[222:225], v248 offset:17408
	ds_read_b128 v[210:213], v248 offset:18432
	ds_read_b128 v[214:217], v248 offset:19456
	ds_read_b128 v[202:205], v248 offset:20480
	ds_read_b128 v[206:209], v248 offset:21504
	ds_read_b128 v[194:197], v248 offset:22528
	ds_read_b128 v[198:201], v248 offset:23552
	s_and_b64 s[30:31], s[28:29], exec
	s_cselect_b32 s4, 0, s4
	s_cselect_b32 s5, 0, 0
	s_add_u32 s30, s54, s4
	s_mov_b32 m0, s35
	s_addc_u32 s31, s55, s5
	global_load_lds_dwordx4 v226, s[30:31]
	s_mov_b32 m0, s36
	v_mov_b32_e32 v227, v231
	global_load_lds_dwordx4 v228, s[30:31]
	s_waitcnt vmcnt(12)
	s_waitcnt lgkmcnt(0)
	v_lshl_add_u64 v[238:239], s[30:31], 0, v[226:227]
	v_mov_b32_e32 v229, v231
	v_cndmask_b32_e64 v227, 0, 1, s[24:25]
	v_lshl_add_u64 v[236:237], s[30:31], 0, v[228:229]
	v_cmp_ne_u32_e64 s[4:5], 1, v227
	s_andn2_b64 vcc, exec, s[24:25]
	s_barrier
; #define PG8_STAGE_A(bufoff, V0, V1, kb) do { \
;         __builtin_amdgcn_global_load_lds((const unsigned*)((Abase + (kb)) + (V0)), (LAS unsigned*)(lds + (bufoff) + ldsw), 16, 0, 0); \
;         __builtin_amdgcn_global_load_lds((const unsigned*)((Abase + (kb)) + (V1)), (LAS unsigned*)(lds + (bufoff) + ldsw + 8192), 16, 0, 0); } while (0)
; #define PG8_LDA(dst, b, h) do { _Pragma("unroll") for (int m = 0; m < 4; ++m) _Pragma("unroll") for (int k = 0; k < 2; ++k) dst[m][k] = *(const LAS bf16x8*)(lds + PG8_SA(b, h) + aoff + m * 2048 + k * 1024); } while (0)
; #define PG8_LDB(dst, b, h) do { _Pragma("unroll") for (int n = 0; n < 2; ++n) _Pragma("unroll") for (int k = 0; k < 2; ++k) dst[n][k] = *(const LAS bf16x8*)(lds + PG8_SB(b, h) + boff + n * 2048 + k * 1024); } while (0)
; #define PG8_MMA(ai, bj, At, Bt) do { __builtin_amdgcn_s_setprio(1); _Pragma("unroll") for (int m = 0; m < 4; ++m) _Pragma("unroll") for (int n = 0; n < 2; ++n) _Pragma("unroll") for (int k = 0; k < 2; ++k) \
;         acc[ai][bj][m][n] = __builtin_amdgcn_mfma_f32_16x16x32_bf16(Bt[n][k], At[m][k], acc[ai][bj][m][n], 0, 0, 0); __builtin_amdgcn_s_setprio(0); } while (0)
; #define PG8_WAIT_V(n) asm volatile("s_waitcnt vmcnt(" #n ")" ::: "memory")
; #define PG8_WAIT_L(n) asm volatile("s_waitcnt lgkmcnt(" #n ")" ::: "memory")
; #define PG8_BAR __builtin_amdgcn_s_barrier()
; #define PG8_SCHED __builtin_amdgcn_sched_barrier(0)
; template <class Epi, class Sched, bool ALIGN_EPI>
; __device__ __forceinline__ void gemm_phase(LAS unsigned char* lds, const Gemm g, const Sched& S, const Epi& E) {
;     ...
;             PG8_WAIT_V(12); PG8_WAIT_L(0); PG8_BAR; if (half1) { PG8_MMA(1, 0, At, B0); PG8_MMA(1, 1, At, B1); } PG8_BAR; PG8_SCHED;
;             PG8_LDB(B0, 1, 0); PG8_LDB(B1, 1, 1); PG8_SCHED; PG8_LDA(At, 1, 0); PG8_STAGE_A(PG8_SA(0, 1), vc10, vc11, kb2);
;             PG8_WAIT_V(12); PG8_WAIT_L(0); PG8_BAR; PG8_MMA(0, 0, At, B0); PG8_MMA(0, 1, At, B1); PG8_BAR; PG8_SCHED;
	s_cbranch_vccnz .LBB0_2450
	s_setprio 1
	s_waitcnt lgkmcnt(0)
	v_mfma_f32_16x16x32_bf16 v[94:97], v[178:181], v[218:221], v[94:97]
	v_mfma_f32_16x16x32_bf16 v[90:93], v[186:189], v[218:221], v[90:93]
	v_mfma_f32_16x16x32_bf16 v[78:81], v[178:181], v[210:213], v[78:81]
	v_mfma_f32_16x16x32_bf16 v[74:77], v[186:189], v[210:213], v[74:77]
	v_mfma_f32_16x16x32_bf16 v[62:65], v[178:181], v[202:205], v[62:65]
	v_mfma_f32_16x16x32_bf16 v[58:61], v[186:189], v[202:205], v[58:61]
	v_mfma_f32_16x16x32_bf16 v[46:49], v[178:181], v[194:197], v[46:49]
	v_mfma_f32_16x16x32_bf16 v[42:45], v[186:189], v[194:197], v[42:45]
	v_mfma_f32_16x16x32_bf16 v[94:97], v[182:185], v[222:225], v[94:97]
	v_mfma_f32_16x16x32_bf16 v[90:93], v[190:193], v[222:225], v[90:93]
	v_mfma_f32_16x16x32_bf16 v[78:81], v[182:185], v[214:217], v[78:81]
	v_mfma_f32_16x16x32_bf16 v[74:77], v[190:193], v[214:217], v[74:77]
	v_mfma_f32_16x16x32_bf16 v[62:65], v[182:185], v[206:209], v[62:65]
	v_mfma_f32_16x16x32_bf16 v[58:61], v[190:193], v[206:209], v[58:61]
	v_mfma_f32_16x16x32_bf16 v[46:49], v[182:185], v[198:201], v[46:49]
	v_mfma_f32_16x16x32_bf16 v[42:45], v[190:193], v[198:201], v[42:45]
	s_setprio 0
	s_setprio 1
	v_mfma_f32_16x16x32_bf16 v[86:89], v[162:165], v[218:221], v[86:89]
	v_mfma_f32_16x16x32_bf16 v[82:85], v[170:173], v[218:221], v[82:85]
	v_mfma_f32_16x16x32_bf16 v[70:73], v[162:165], v[210:213], v[70:73]
	v_mfma_f32_16x16x32_bf16 v[66:69], v[170:173], v[210:213], v[66:69]
	v_mfma_f32_16x16x32_bf16 v[54:57], v[162:165], v[202:205], v[54:57]
	v_mfma_f32_16x16x32_bf16 v[50:53], v[170:173], v[202:205], v[50:53]
	v_mfma_f32_16x16x32_bf16 v[38:41], v[162:165], v[194:197], v[38:41]
	v_mfma_f32_16x16x32_bf16 v[34:37], v[170:173], v[194:197], v[34:37]
	v_mfma_f32_16x16x32_bf16 v[86:89], v[166:169], v[222:225], v[86:89]
	v_mfma_f32_16x16x32_bf16 v[82:85], v[174:177], v[222:225], v[82:85]
	v_mfma_f32_16x16x32_bf16 v[70:73], v[166:169], v[214:217], v[70:73]
	v_mfma_f32_16x16x32_bf16 v[66:69], v[174:177], v[214:217], v[66:69]
	v_mfma_f32_16x16x32_bf16 v[54:57], v[166:169], v[206:209], v[54:57]
	v_mfma_f32_16x16x32_bf16 v[50:53], v[174:177], v[206:209], v[50:53]
	v_mfma_f32_16x16x32_bf16 v[38:41], v[166:169], v[198:201], v[38:41]
	v_mfma_f32_16x16x32_bf16 v[34:37], v[174:177], v[198:201], v[34:37]
	s_setprio 0
.LBB0_2450:
	v_cndmask_b32_e64 v232, v232, v252, s[28:29]
	v_cndmask_b32_e64 v230, v230, v251, s[28:29]
	s_barrier
	v_add_u32_e32 v162, 0x18000, v247
	v_add_u32_e32 v174, 0x1c000, v247
	ds_read_b128 v[178:181], v162
	ds_read_b128 v[182:185], v162 offset:1024
	ds_read_b128 v[186:189], v162 offset:2048
	ds_read_b128 v[190:193], v162 offset:3072
	ds_read_b128 v[162:165], v174
	ds_read_b128 v[166:169], v174 offset:1024
	ds_read_b128 v[170:173], v174 offset:2048
	ds_read_b128 v[174:177], v174 offset:3072
	s_mov_b32 m0, s37
	s_waitcnt lgkmcnt(0)
	ds_read_b128 v[194:197], v248 offset:32768
	ds_read_b128 v[198:201], v248 offset:33792
	ds_read_b128 v[202:205], v248 offset:34816
	ds_read_b128 v[206:209], v248 offset:35840
	ds_read_b128 v[210:213], v248 offset:36864
	ds_read_b128 v[214:217], v248 offset:37888
	ds_read_b128 v[218:221], v248 offset:38912
	ds_read_b128 v[222:225], v248 offset:39936
	global_load_lds_dwordx4 v230, s[30:31]
	s_mov_b32 m0, s38
	s_nop 0
	global_load_lds_dwordx4 v232, s[30:31]
	s_waitcnt vmcnt(12)
	s_waitcnt lgkmcnt(0)
	s_barrier
	s_setprio 1
	s_waitcnt lgkmcnt(0)
	v_mfma_f32_16x16x32_bf16 v[158:161], v[178:181], v[194:197], v[158:161]
	v_mfma_f32_16x16x32_bf16 v[154:157], v[186:189], v[194:197], v[154:157]
	v_mfma_f32_16x16x32_bf16 v[142:145], v[178:181], v[202:205], v[142:145]
	v_mfma_f32_16x16x32_bf16 v[138:141], v[186:189], v[202:205], v[138:141]
	v_mfma_f32_16x16x32_bf16 v[126:129], v[178:181], v[210:213], v[126:129]
	v_mfma_f32_16x16x32_bf16 v[122:125], v[186:189], v[210:213], v[122:125]
	v_mfma_f32_16x16x32_bf16 v[110:113], v[178:181], v[218:221], v[110:113]
	v_mfma_f32_16x16x32_bf16 v[106:109], v[186:189], v[218:221], v[106:109]
	v_mfma_f32_16x16x32_bf16 v[158:161], v[182:185], v[198:201], v[158:161]
	v_mfma_f32_16x16x32_bf16 v[154:157], v[190:193], v[198:201], v[154:157]
	v_mfma_f32_16x16x32_bf16 v[142:145], v[182:185], v[206:209], v[142:145]
	v_mfma_f32_16x16x32_bf16 v[138:141], v[190:193], v[206:209], v[138:141]
	v_mfma_f32_16x16x32_bf16 v[126:129], v[182:185], v[214:217], v[126:129]
	v_mfma_f32_16x16x32_bf16 v[122:125], v[190:193], v[214:217], v[122:125]
	v_mfma_f32_16x16x32_bf16 v[110:113], v[182:185], v[222:225], v[110:113]
	v_mfma_f32_16x16x32_bf16 v[106:109], v[190:193], v[222:225], v[106:109]
	s_setprio 0
	s_setprio 1
	v_mfma_f32_16x16x32_bf16 v[150:153], v[162:165], v[194:197], v[150:153]
	v_mfma_f32_16x16x32_bf16 v[146:149], v[170:173], v[194:197], v[146:149]
	v_mfma_f32_16x16x32_bf16 v[134:137], v[162:165], v[202:205], v[134:137]
	v_mfma_f32_16x16x32_bf16 v[130:133], v[170:173], v[202:205], v[130:133]
	v_mfma_f32_16x16x32_bf16 v[118:121], v[162:165], v[210:213], v[118:121]
	v_mfma_f32_16x16x32_bf16 v[114:117], v[170:173], v[210:213], v[114:117]
	v_mfma_f32_16x16x32_bf16 v[102:105], v[162:165], v[218:221], v[102:105]
	v_mfma_f32_16x16x32_bf16 v[98:101], v[170:173], v[218:221], v[98:101]
	v_mfma_f32_16x16x32_bf16 v[150:153], v[166:169], v[198:201], v[150:153]
	v_mfma_f32_16x16x32_bf16 v[146:149], v[174:177], v[198:201], v[146:149]
	v_mfma_f32_16x16x32_bf16 v[134:137], v[166:169], v[206:209], v[134:137]
	v_mfma_f32_16x16x32_bf16 v[130:133], v[174:177], v[206:209], v[130:133]
	v_mfma_f32_16x16x32_bf16 v[118:121], v[166:169], v[214:217], v[118:121]
	v_mfma_f32_16x16x32_bf16 v[114:117], v[174:177], v[214:217], v[114:117]
	v_mfma_f32_16x16x32_bf16 v[102:105], v[166:169], v[222:225], v[102:105]
	v_mfma_f32_16x16x32_bf16 v[98:101], v[174:177], v[222:225], v[98:101]
	s_setprio 0
	s_barrier
; #define PG8_BWAIT(n) asm volatile("s_waitcnt vmcnt(" #n ")" : "+v"(bv[0]), "+v"(bv[1]), "+v"(bv[2]), "+v"(bv[3]), "+v"(bv[4]), "+v"(bv[5]), "+v"(bv[6]), "+v"(bv[7]) :: "memory")
; #define PG8_STAGE_A(bufoff, V0, V1, kb) do { \
;         __builtin_amdgcn_global_load_lds((const unsigned*)((Abase + (kb)) + (V0)), (LAS unsigned*)(lds + (bufoff) + ldsw), 16, 0, 0); \
;         __builtin_amdgcn_global_load_lds((const unsigned*)((Abase + (kb)) + (V1)), (LAS unsigned*)(lds + (bufoff) + ldsw + 8192), 16, 0, 0); } while (0)
; #define PG8_LDA(dst, b, h) do { _Pragma("unroll") for (int m = 0; m < 4; ++m) _Pragma("unroll") for (int k = 0; k < 2; ++k) dst[m][k] = *(const LAS bf16x8*)(lds + PG8_SA(b, h) + aoff + m * 2048 + k * 1024); } while (0)
; #define PG8_MMA(ai, bj, At, Bt) do { __builtin_amdgcn_s_setprio(1); _Pragma("unroll") for (int m = 0; m < 4; ++m) _Pragma("unroll") for (int n = 0; n < 2; ++n) _Pragma("unroll") for (int k = 0; k < 2; ++k) \
;         acc[ai][bj][m][n] = __builtin_amdgcn_mfma_f32_16x16x32_bf16(Bt[n][k], At[m][k], acc[ai][bj][m][n], 0, 0, 0); __builtin_amdgcn_s_setprio(0); } while (0)
; #define PG8_WAIT_V(n) asm volatile("s_waitcnt vmcnt(" #n ")" ::: "memory")
; #define PG8_WAIT_L(n) asm volatile("s_waitcnt lgkmcnt(" #n ")" ::: "memory")
; #define PG8_BAR __builtin_amdgcn_s_barrier()
; #define PG8_SCHED __builtin_amdgcn_sched_barrier(0)
; template <class Epi, class Sched, bool ALIGN_EPI>
; __device__ __forceinline__ void gemm_phase(LAS unsigned char* lds, const Gemm g, const Sched& S, const Epi& E) {
;     ...
;             PG8_BWAIT(2); PG8_BCOMMIT(1); PG8_SCHED; PG8_LDA(At, 1, 1); PG8_BISSUE(t + 4 >= nt ? pbn + (size_t)(t + 4 - nt) * 64 * Sched::LDN : pbc + (size_t)(t + 4) * 64 * Sched::LDN); PG8_STAGE_A(PG8_SA(1, 0), vc00, vc01, kb2 + 128u);
;             PG8_WAIT_V(12); PG8_WAIT_L(0); PG8_BAR; if (half1) { PG8_MMA(1, 0, At, B0); PG8_MMA(1, 1, At, B1); } PG8_BAR; PG8_SCHED;
	s_lshl_b32 s10, s50, 16
	s_lshl_b64 s[28:29], s[10:11], 2
	s_add_u32 s28, s47, s28
	s_addc_u32 s29, s21, s29
	s_add_u32 s30, s28, 0x1000
	s_waitcnt vmcnt(2)
	s_nop 0
	v_cvt_pk_bf16_f32 v194, v2, v6
	v_cvt_pk_bf16_f32 v198, v3, v7
	v_cvt_pk_bf16_f32 v202, v4, v8
	v_cvt_pk_bf16_f32 v206, v5, v9
	global_load_dwordx4 v[2:5], v240, s[28:29] offset:0
	s_addc_u32 s31, s29, 0
	global_load_dwordx4 v[6:9], v240, s[30:31] offset:0
	v_cvt_pk_bf16_f32 v195, v10, v14
	v_cvt_pk_bf16_f32 v199, v11, v15
	v_cvt_pk_bf16_f32 v203, v12, v16
	v_cvt_pk_bf16_f32 v207, v13, v17
	s_add_u32 s30, s28, 0x2000
	s_addc_u32 s31, s29, 0
	global_load_dwordx4 v[10:13], v240, s[30:31] offset:0
	s_add_u32 s30, s28, 0x3000
	s_addc_u32 s31, s29, 0
	global_load_dwordx4 v[14:17], v240, s[30:31] offset:0
	v_cvt_pk_bf16_f32 v196, v18, v22
	v_cvt_pk_bf16_f32 v200, v19, v23
	v_cvt_pk_bf16_f32 v204, v20, v24
	v_cvt_pk_bf16_f32 v208, v21, v25
	s_add_u32 s30, s28, 0x4000
	s_addc_u32 s31, s29, 0
	global_load_dwordx4 v[18:21], v240, s[30:31] offset:0
	s_add_u32 s30, s28, 0x5000
	s_addc_u32 s31, s29, 0
	global_load_dwordx4 v[22:25], v240, s[30:31] offset:0
	v_cvt_pk_bf16_f32 v197, v26, v30
	v_cvt_pk_bf16_f32 v201, v27, v31
	v_cvt_pk_bf16_f32 v205, v28, v32
	v_cvt_pk_bf16_f32 v209, v29, v33
	s_add_u32 s30, s28, 0x6000
	s_addc_u32 s31, s29, 0
	global_load_dwordx4 v[26:29], v240, s[30:31] offset:0
	s_add_u32 s28, s28, 0x7000
	s_mov_b32 m0, s39
	s_addc_u32 s29, s29, 0
	global_load_dwordx4 v[30:33], v240, s[28:29] offset:0
	v_add_u32_e32 v210, 0x18000, v242
	v_xor_b32_e32 v211, 64, v210
	v_xor_b32_e32 v212, 0x80, v210
	v_xor_b32_e32 v213, 0xc0, v210
	ds_write_b128 v210, v[194:197]
	ds_write_b128 v211, v[198:201]
	ds_write_b128 v212, v[202:205]
	ds_write_b128 v213, v[206:209]
	ds_read_b128 v[218:221], v248 offset:49152
	ds_read_b128 v[222:225], v248 offset:50176
	ds_read_b128 v[210:213], v248 offset:51200
	ds_read_b128 v[214:217], v248 offset:52224
	ds_read_b128 v[202:205], v248 offset:53248
	ds_read_b128 v[206:209], v248 offset:54272
	ds_read_b128 v[194:197], v248 offset:55296
	ds_read_b128 v[198:201], v248 offset:56320
	v_lshl_add_u64 v[238:239], v[238:239], 0, s[16:17]
	global_load_lds_dwordx4 v[238:239], off
	v_lshl_add_u64 v[236:237], v[236:237], 0, s[16:17]
	s_mov_b32 m0, s40
	s_and_b64 vcc, exec, s[4:5]
	global_load_lds_dwordx4 v[236:237], off
	s_waitcnt vmcnt(12)
	s_waitcnt lgkmcnt(0)
	s_barrier
	s_cbranch_vccnz .LBB0_2447
	s_setprio 1
	s_waitcnt lgkmcnt(0)
	v_mfma_f32_16x16x32_bf16 v[94:97], v[178:181], v[218:221], v[94:97]
	v_mfma_f32_16x16x32_bf16 v[90:93], v[186:189], v[218:221], v[90:93]
	v_mfma_f32_16x16x32_bf16 v[78:81], v[178:181], v[210:213], v[78:81]
	v_mfma_f32_16x16x32_bf16 v[74:77], v[186:189], v[210:213], v[74:77]
	v_mfma_f32_16x16x32_bf16 v[62:65], v[178:181], v[202:205], v[62:65]
	v_mfma_f32_16x16x32_bf16 v[58:61], v[186:189], v[202:205], v[58:61]
	v_mfma_f32_16x16x32_bf16 v[46:49], v[178:181], v[194:197], v[46:49]
	v_mfma_f32_16x16x32_bf16 v[42:45], v[186:189], v[194:197], v[42:45]
	v_mfma_f32_16x16x32_bf16 v[94:97], v[182:185], v[222:225], v[94:97]
	v_mfma_f32_16x16x32_bf16 v[90:93], v[190:193], v[222:225], v[90:93]
	v_mfma_f32_16x16x32_bf16 v[78:81], v[182:185], v[214:217], v[78:81]
	v_mfma_f32_16x16x32_bf16 v[74:77], v[190:193], v[214:217], v[74:77]
	v_mfma_f32_16x16x32_bf16 v[62:65], v[182:185], v[206:209], v[62:65]
	v_mfma_f32_16x16x32_bf16 v[58:61], v[190:193], v[206:209], v[58:61]
	v_mfma_f32_16x16x32_bf16 v[46:49], v[182:185], v[198:201], v[46:49]
	v_mfma_f32_16x16x32_bf16 v[42:45], v[190:193], v[198:201], v[42:45]
	s_setprio 0
	s_setprio 1
	v_mfma_f32_16x16x32_bf16 v[86:89], v[162:165], v[218:221], v[86:89]
	v_mfma_f32_16x16x32_bf16 v[82:85], v[170:173], v[218:221], v[82:85]
	v_mfma_f32_16x16x32_bf16 v[70:73], v[162:165], v[210:213], v[70:73]
	v_mfma_f32_16x16x32_bf16 v[66:69], v[170:173], v[210:213], v[66:69]
	v_mfma_f32_16x16x32_bf16 v[54:57], v[162:165], v[202:205], v[54:57]
	v_mfma_f32_16x16x32_bf16 v[50:53], v[170:173], v[202:205], v[50:53]
	v_mfma_f32_16x16x32_bf16 v[38:41], v[162:165], v[194:197], v[38:41]
	v_mfma_f32_16x16x32_bf16 v[34:37], v[170:173], v[194:197], v[34:37]
	v_mfma_f32_16x16x32_bf16 v[86:89], v[166:169], v[222:225], v[86:89]
	v_mfma_f32_16x16x32_bf16 v[82:85], v[174:177], v[222:225], v[82:85]
	v_mfma_f32_16x16x32_bf16 v[70:73], v[166:169], v[214:217], v[70:73]
	v_mfma_f32_16x16x32_bf16 v[66:69], v[174:177], v[214:217], v[66:69]
	v_mfma_f32_16x16x32_bf16 v[54:57], v[166:169], v[206:209], v[54:57]
	v_mfma_f32_16x16x32_bf16 v[50:53], v[174:177], v[206:209], v[50:53]
	v_mfma_f32_16x16x32_bf16 v[38:41], v[166:169], v[198:201], v[38:41]
	v_mfma_f32_16x16x32_bf16 v[34:37], v[174:177], v[198:201], v[34:37]
	s_setprio 0
	s_branch .LBB0_2447

; #define PG8_BWAIT(n) asm volatile("s_waitcnt vmcnt(" #n ")" : "+v"(bv[0]), "+v"(bv[1]), "+v"(bv[2]), "+v"(bv[3]), "+v"(bv[4]), "+v"(bv[5]), "+v"(bv[6]), "+v"(bv[7]) :: "memory")
; #define PG8_STAGE_A(bufoff, V0, V1, kb) do { \
;         __builtin_amdgcn_global_load_lds((const unsigned*)((Abase + (kb)) + (V0)), (LAS unsigned*)(lds + (bufoff) + ldsw), 16, 0, 0); \
;         __builtin_amdgcn_global_load_lds((const unsigned*)((Abase + (kb)) + (V1)), (LAS unsigned*)(lds + (bufoff) + ldsw + 8192), 16, 0, 0); } while (0)
; #define PG8_LDA(dst, b, h) do { _Pragma("unroll") for (int m = 0; m < 4; ++m) _Pragma("unroll") for (int k = 0; k < 2; ++k) dst[m][k] = *(const LAS bf16x8*)(lds + PG8_SA(b, h) + aoff + m * 2048 + k * 1024); } while (0)
; #define PG8_LDB(dst, b, h) do { _Pragma("unroll") for (int n = 0; n < 2; ++n) _Pragma("unroll") for (int k = 0; k < 2; ++k) dst[n][k] = *(const LAS bf16x8*)(lds + PG8_SB(b, h) + boff + n * 2048 + k * 1024); } while (0)
; #define PG8_MMA(ai, bj, At, Bt) do { __builtin_amdgcn_s_setprio(1); _Pragma("unroll") for (int m = 0; m < 4; ++m) _Pragma("unroll") for (int n = 0; n < 2; ++n) _Pragma("unroll") for (int k = 0; k < 2; ++k) \
;         acc[ai][bj][m][n] = __builtin_amdgcn_mfma_f32_16x16x32_bf16(Bt[n][k], At[m][k], acc[ai][bj][m][n], 0, 0, 0); __builtin_amdgcn_s_setprio(0); } while (0)
; #define PG8_WAIT_V(n) asm volatile("s_waitcnt vmcnt(" #n ")" ::: "memory")
; #define PG8_WAIT_L(n) asm volatile("s_waitcnt lgkmcnt(" #n ")" ::: "memory")
; #define PG8_BAR __builtin_amdgcn_s_barrier()
; #define PG8_SCHED __builtin_amdgcn_sched_barrier(0)
; template <class Epi, class Sched, bool ALIGN_EPI>
; __device__ __forceinline__ void gemm_phase(LAS unsigned char* lds, const Gemm g, const Sched& S, const Epi& E) {
;     ...
;             PG8_LDB(B0, 0, 0); PG8_LDB(B1, 0, 1); PG8_SCHED; PG8_LDA(At, 0, 0); PG8_STAGE_A(PG8_SA(1, 1), vc10, vc11, kb1);
;             PG8_WAIT_V(12); PG8_WAIT_L(0); PG8_BAR; PG8_MMA(0, 0, At, B0); PG8_MMA(0, 1, At, B1); PG8_BAR; PG8_SCHED;
;             if (last) { vc10 = vn10; vc11 = vn11; }
;             PG8_BWAIT(2); PG8_BCOMMIT(0); PG8_SCHED; PG8_LDA(At, 0, 1); PG8_BISSUE(t + 3 >= nt ? pbn + (size_t)(t + 3 - nt) * 64 * Sched::LDN : pbc + (size_t)(t + 3) * 64 * Sched::LDN); PG8_STAGE_A(PG8_SA(0, 0), vc00, vc01, kb2);
.LBB0_4711:
	v_add_u32_e32 v162, 0x10000, v240
	v_add_u32_e32 v174, 0x14000, v240
	ds_read_b128 v[178:181], v162
	ds_read_b128 v[182:185], v162 offset:1024
	ds_read_b128 v[186:189], v162 offset:2048
	ds_read_b128 v[190:193], v162 offset:3072
	ds_read_b128 v[162:165], v174
	ds_read_b128 v[166:169], v174 offset:1024
	ds_read_b128 v[170:173], v174 offset:2048
	ds_read_b128 v[174:177], v174 offset:3072
	s_add_i32 s54, s53, 2
	s_add_i32 m0, s40, 0xc000
	s_add_u32 s2, s90, s22
	s_addc_u32 s3, s91, s23
	s_waitcnt lgkmcnt(0)
	ds_read_b128 v[194:197], v241
	ds_read_b128 v[198:201], v241 offset:1024
	ds_read_b128 v[202:205], v241 offset:2048
	ds_read_b128 v[206:209], v241 offset:3072
	ds_read_b128 v[210:213], v241 offset:4096
	ds_read_b128 v[214:217], v241 offset:5120
	ds_read_b128 v[218:221], v241 offset:6144
	ds_read_b128 v[222:225], v241 offset:7168
	global_load_lds_dwordx4 v233, s[2:3]
	s_add_i32 m0, s40, 0xe000
	s_nop 0
	global_load_lds_dwordx4 v234, s[2:3]
	s_waitcnt vmcnt(12)
	s_waitcnt lgkmcnt(0)
	s_barrier
	s_setprio 1
	s_waitcnt lgkmcnt(0)
	v_mfma_f32_16x16x32_bf16 v[158:161], v[178:181], v[194:197], v[158:161]
	v_mfma_f32_16x16x32_bf16 v[154:157], v[186:189], v[194:197], v[154:157]
	v_mfma_f32_16x16x32_bf16 v[142:145], v[178:181], v[202:205], v[142:145]
	v_mfma_f32_16x16x32_bf16 v[138:141], v[186:189], v[202:205], v[138:141]
	v_mfma_f32_16x16x32_bf16 v[126:129], v[178:181], v[210:213], v[126:129]
	v_mfma_f32_16x16x32_bf16 v[122:125], v[186:189], v[210:213], v[122:125]
	v_mfma_f32_16x16x32_bf16 v[110:113], v[178:181], v[218:221], v[110:113]
	v_mfma_f32_16x16x32_bf16 v[106:109], v[186:189], v[218:221], v[106:109]
	v_mfma_f32_16x16x32_bf16 v[158:161], v[182:185], v[198:201], v[158:161]
	v_mfma_f32_16x16x32_bf16 v[154:157], v[190:193], v[198:201], v[154:157]
	v_mfma_f32_16x16x32_bf16 v[142:145], v[182:185], v[206:209], v[142:145]
	v_mfma_f32_16x16x32_bf16 v[138:141], v[190:193], v[206:209], v[138:141]
	v_mfma_f32_16x16x32_bf16 v[126:129], v[182:185], v[214:217], v[126:129]
	v_mfma_f32_16x16x32_bf16 v[122:125], v[190:193], v[214:217], v[122:125]
	v_mfma_f32_16x16x32_bf16 v[110:113], v[182:185], v[222:225], v[110:113]
	v_mfma_f32_16x16x32_bf16 v[106:109], v[190:193], v[222:225], v[106:109]
	s_setprio 0
	s_setprio 1
	v_mfma_f32_16x16x32_bf16 v[150:153], v[162:165], v[194:197], v[150:153]
	v_mfma_f32_16x16x32_bf16 v[146:149], v[170:173], v[194:197], v[146:149]
	v_mfma_f32_16x16x32_bf16 v[134:137], v[162:165], v[202:205], v[134:137]
	v_mfma_f32_16x16x32_bf16 v[130:133], v[170:173], v[202:205], v[130:133]
	v_mfma_f32_16x16x32_bf16 v[118:121], v[162:165], v[210:213], v[118:121]
	v_mfma_f32_16x16x32_bf16 v[114:117], v[170:173], v[210:213], v[114:117]
	v_mfma_f32_16x16x32_bf16 v[102:105], v[162:165], v[218:221], v[102:105]
	v_mfma_f32_16x16x32_bf16 v[98:101], v[170:173], v[218:221], v[98:101]
	v_mfma_f32_16x16x32_bf16 v[150:153], v[166:169], v[198:201], v[150:153]
	v_mfma_f32_16x16x32_bf16 v[146:149], v[174:177], v[198:201], v[146:149]
	v_mfma_f32_16x16x32_bf16 v[134:137], v[166:169], v[206:209], v[134:137]
	v_mfma_f32_16x16x32_bf16 v[130:133], v[174:177], v[206:209], v[130:133]
	v_mfma_f32_16x16x32_bf16 v[118:121], v[166:169], v[214:217], v[118:121]
	v_mfma_f32_16x16x32_bf16 v[114:117], v[174:177], v[214:217], v[114:117]
	v_mfma_f32_16x16x32_bf16 v[102:105], v[166:169], v[222:225], v[102:105]
	v_mfma_f32_16x16x32_bf16 v[98:101], v[174:177], v[222:225], v[98:101]
	s_setprio 0
	s_barrier
	s_cmp_lt_u32 s54, 13
	s_mov_b64 s[4:5], -1
	s_cbranch_scc0 .LBB0_4713
	s_add_u32 s2, s20, 0x30000
	s_addc_u32 s3, s21, 0
	s_mov_b64 s[4:5], 0

; #define PG8_BWAIT(n) asm volatile("s_waitcnt vmcnt(" #n ")" : "+v"(bv[0]), "+v"(bv[1]), "+v"(bv[2]), "+v"(bv[3]), "+v"(bv[4]), "+v"(bv[5]), "+v"(bv[6]), "+v"(bv[7]) :: "memory")
; #define PG8_STAGE_A(bufoff, V0, V1, kb) do { \
;         __builtin_amdgcn_global_load_lds((const unsigned*)((Abase + (kb)) + (V0)), (LAS unsigned*)(lds + (bufoff) + ldsw), 16, 0, 0); \
;         __builtin_amdgcn_global_load_lds((const unsigned*)((Abase + (kb)) + (V1)), (LAS unsigned*)(lds + (bufoff) + ldsw + 8192), 16, 0, 0); } while (0)
; #define PG8_LDA(dst, b, h) do { _Pragma("unroll") for (int m = 0; m < 4; ++m) _Pragma("unroll") for (int k = 0; k < 2; ++k) dst[m][k] = *(const LAS bf16x8*)(lds + PG8_SA(b, h) + aoff + m * 2048 + k * 1024); } while (0)
; #define PG8_MMA(ai, bj, At, Bt) do { __builtin_amdgcn_s_setprio(1); _Pragma("unroll") for (int m = 0; m < 4; ++m) _Pragma("unroll") for (int n = 0; n < 2; ++n) _Pragma("unroll") for (int k = 0; k < 2; ++k) \
;         acc[ai][bj][m][n] = __builtin_amdgcn_mfma_f32_16x16x32_bf16(Bt[n][k], At[m][k], acc[ai][bj][m][n], 0, 0, 0); __builtin_amdgcn_s_setprio(0); } while (0)
; #define PG8_WAIT_V(n) asm volatile("s_waitcnt vmcnt(" #n ")" ::: "memory")
; #define PG8_WAIT_L(n) asm volatile("s_waitcnt lgkmcnt(" #n ")" ::: "memory")
; #define PG8_BAR __builtin_amdgcn_s_barrier()
; #define PG8_SCHED __builtin_amdgcn_sched_barrier(0)
; template <class Epi, class Sched, bool ALIGN_EPI>
; __device__ __forceinline__ void gemm_phase(LAS unsigned char* lds, const Gemm g, const Sched& S, const Epi& E) {
;     ...
;             PG8_BWAIT(2); PG8_BCOMMIT(0); PG8_SCHED; PG8_LDA(At, 0, 1); PG8_BISSUE(t + 3 >= nt ? pbn + (size_t)(t + 3 - nt) * 64 * Sched::LDN : pbc + (size_t)(t + 3) * 64 * Sched::LDN); PG8_STAGE_A(PG8_SA(0, 0), vc00, vc01, kb2);
;             PG8_WAIT_V(12); PG8_WAIT_L(0); PG8_BAR; if (half1) { PG8_MMA(1, 0, At, B0); PG8_MMA(1, 1, At, B1); } PG8_BAR; PG8_SCHED;
.LBB0_4715:
	s_add_i32 s8, s22, 0xe8940080
	s_cmp_eq_u32 s53, 12
	s_waitcnt vmcnt(2)
	s_nop 0
	v_cvt_pk_bf16_f32 v194, v2, v6
	v_cvt_pk_bf16_f32 v198, v3, v7
	v_cvt_pk_bf16_f32 v202, v4, v8
	v_cvt_pk_bf16_f32 v206, v5, v9
	global_load_dwordx4 v[2:5], v232, s[2:3] offset:0
	s_cselect_b64 s[4:5], -1, 0
	global_load_dwordx4 v[6:9], v232, s[2:3] offset:0x400
	v_cvt_pk_bf16_f32 v195, v10, v14
	v_cvt_pk_bf16_f32 v199, v11, v15
	v_cvt_pk_bf16_f32 v203, v12, v16
	v_cvt_pk_bf16_f32 v207, v13, v17
	s_and_b64 s[26:27], s[4:5], exec
	global_load_dwordx4 v[10:13], v232, s[2:3] offset:0x800
	s_cselect_b32 s8, 0, s8
	global_load_dwordx4 v[14:17], v232, s[2:3] offset:0xc00
	v_cvt_pk_bf16_f32 v196, v18, v22
	v_cvt_pk_bf16_f32 v200, v19, v23
	v_cvt_pk_bf16_f32 v204, v20, v24
	v_cvt_pk_bf16_f32 v208, v21, v25
	s_add_u32 s2, s2, 0x1000
	s_addc_u32 s3, s3, 0
	global_load_dwordx4 v[18:21], v232, s[2:3] offset:0
	global_load_dwordx4 v[22:25], v232, s[2:3] offset:0x400
	v_cvt_pk_bf16_f32 v197, v26, v30
	v_cvt_pk_bf16_f32 v201, v27, v31
	v_cvt_pk_bf16_f32 v205, v28, v32
	v_cvt_pk_bf16_f32 v209, v29, v33
	global_load_dwordx4 v[26:29], v232, s[2:3] offset:0x800
	global_load_dwordx4 v[30:33], v232, s[2:3] offset:0xc00
	v_add_u32_e32 v210, 0x10000, v235
	v_xor_b32_e32 v211, 64, v210
	v_xor_b32_e32 v212, 0x80, v210
	v_xor_b32_e32 v213, 0xc0, v210
	ds_write_b128 v210, v[194:197]
	ds_write_b128 v211, v[198:201]
	ds_write_b128 v212, v[202:205]
	ds_write_b128 v213, v[206:209]
	ds_read_b128 v[218:221], v241 offset:16384
	ds_read_b128 v[222:225], v241 offset:17408
	ds_read_b128 v[210:213], v241 offset:18432
	ds_read_b128 v[214:217], v241 offset:19456
	ds_read_b128 v[202:205], v241 offset:20480
	ds_read_b128 v[206:209], v241 offset:21504
	ds_read_b128 v[194:197], v241 offset:22528
	ds_read_b128 v[198:201], v241 offset:23552
	v_readlane_b32 s2, v255, 13
	v_readlane_b32 s3, v255, 14
	s_add_u32 s26, s2, s8
	s_mov_b32 m0, s40
	v_cndmask_b32_e64 v226, v226, v242, s[4:5]
	s_addc_u32 s27, s3, 0
	v_cndmask_b32_e64 v228, v228, v243, s[4:5]
	global_load_lds_dwordx4 v226, s[26:27]
	s_mov_b32 m0, s41
	v_cndmask_b32_e64 v229, 0, 1, s[24:25]
	global_load_lds_dwordx4 v228, s[26:27]
	s_waitcnt vmcnt(12)
	s_waitcnt lgkmcnt(0)
	v_cmp_ne_u32_e64 s[2:3], 1, v229
	s_andn2_b64 vcc, exec, s[24:25]
	s_barrier
	s_cbranch_vccnz .LBB0_4717
	s_setprio 1
	s_waitcnt lgkmcnt(0)
	v_mfma_f32_16x16x32_bf16 v[94:97], v[178:181], v[218:221], v[94:97]
	v_mfma_f32_16x16x32_bf16 v[90:93], v[186:189], v[218:221], v[90:93]
	v_mfma_f32_16x16x32_bf16 v[78:81], v[178:181], v[210:213], v[78:81]
	v_mfma_f32_16x16x32_bf16 v[74:77], v[186:189], v[210:213], v[74:77]
	v_mfma_f32_16x16x32_bf16 v[62:65], v[178:181], v[202:205], v[62:65]
	v_mfma_f32_16x16x32_bf16 v[58:61], v[186:189], v[202:205], v[58:61]
	v_mfma_f32_16x16x32_bf16 v[46:49], v[178:181], v[194:197], v[46:49]
	v_mfma_f32_16x16x32_bf16 v[42:45], v[186:189], v[194:197], v[42:45]
	v_mfma_f32_16x16x32_bf16 v[94:97], v[182:185], v[222:225], v[94:97]
	v_mfma_f32_16x16x32_bf16 v[90:93], v[190:193], v[222:225], v[90:93]
	v_mfma_f32_16x16x32_bf16 v[78:81], v[182:185], v[214:217], v[78:81]
	v_mfma_f32_16x16x32_bf16 v[74:77], v[190:193], v[214:217], v[74:77]
	v_mfma_f32_16x16x32_bf16 v[62:65], v[182:185], v[206:209], v[62:65]
	v_mfma_f32_16x16x32_bf16 v[58:61], v[190:193], v[206:209], v[58:61]
	v_mfma_f32_16x16x32_bf16 v[46:49], v[182:185], v[198:201], v[46:49]
	v_mfma_f32_16x16x32_bf16 v[42:45], v[190:193], v[198:201], v[42:45]
	s_setprio 0
	s_setprio 1
	v_mfma_f32_16x16x32_bf16 v[86:89], v[162:165], v[218:221], v[86:89]
	v_mfma_f32_16x16x32_bf16 v[82:85], v[170:173], v[218:221], v[82:85]
	v_mfma_f32_16x16x32_bf16 v[70:73], v[162:165], v[210:213], v[70:73]
	v_mfma_f32_16x16x32_bf16 v[66:69], v[170:173], v[210:213], v[66:69]
	v_mfma_f32_16x16x32_bf16 v[54:57], v[162:165], v[202:205], v[54:57]
	v_mfma_f32_16x16x32_bf16 v[50:53], v[170:173], v[202:205], v[50:53]
	v_mfma_f32_16x16x32_bf16 v[38:41], v[162:165], v[194:197], v[38:41]
	v_mfma_f32_16x16x32_bf16 v[34:37], v[170:173], v[194:197], v[34:37]
	v_mfma_f32_16x16x32_bf16 v[86:89], v[166:169], v[222:225], v[86:89]
	v_mfma_f32_16x16x32_bf16 v[82:85], v[174:177], v[222:225], v[82:85]
	v_mfma_f32_16x16x32_bf16 v[70:73], v[166:169], v[214:217], v[70:73]
	v_mfma_f32_16x16x32_bf16 v[66:69], v[174:177], v[214:217], v[66:69]
	v_mfma_f32_16x16x32_bf16 v[54:57], v[166:169], v[206:209], v[54:57]
	v_mfma_f32_16x16x32_bf16 v[50:53], v[174:177], v[206:209], v[50:53]
	v_mfma_f32_16x16x32_bf16 v[38:41], v[166:169], v[198:201], v[38:41]
	v_mfma_f32_16x16x32_bf16 v[34:37], v[174:177], v[198:201], v[34:37]
	s_setprio 0
; #define PG8_BWAIT(n) asm volatile("s_waitcnt vmcnt(" #n ")" : "+v"(bv[0]), "+v"(bv[1]), "+v"(bv[2]), "+v"(bv[3]), "+v"(bv[4]), "+v"(bv[5]), "+v"(bv[6]), "+v"(bv[7]) :: "memory")
; #define PG8_STAGE_A(bufoff, V0, V1, kb) do { \
;         __builtin_amdgcn_global_load_lds((const unsigned*)((Abase + (kb)) + (V0)), (LAS unsigned*)(lds + (bufoff) + ldsw), 16, 0, 0); \
;         __builtin_amdgcn_global_load_lds((const unsigned*)((Abase + (kb)) + (V1)), (LAS unsigned*)(lds + (bufoff) + ldsw + 8192), 16, 0, 0); } while (0)
; #define PG8_LDA(dst, b, h) do { _Pragma("unroll") for (int m = 0; m < 4; ++m) _Pragma("unroll") for (int k = 0; k < 2; ++k) dst[m][k] = *(const LAS bf16x8*)(lds + PG8_SA(b, h) + aoff + m * 2048 + k * 1024); } while (0)
; #define PG8_LDB(dst, b, h) do { _Pragma("unroll") for (int n = 0; n < 2; ++n) _Pragma("unroll") for (int k = 0; k < 2; ++k) dst[n][k] = *(const LAS bf16x8*)(lds + PG8_SB(b, h) + boff + n * 2048 + k * 1024); } while (0)
; #define PG8_MMA(ai, bj, At, Bt) do { __builtin_amdgcn_s_setprio(1); _Pragma("unroll") for (int m = 0; m < 4; ++m) _Pragma("unroll") for (int n = 0; n < 2; ++n) _Pragma("unroll") for (int k = 0; k < 2; ++k) \
;         acc[ai][bj][m][n] = __builtin_amdgcn_mfma_f32_16x16x32_bf16(Bt[n][k], At[m][k], acc[ai][bj][m][n], 0, 0, 0); __builtin_amdgcn_s_setprio(0); } while (0)
; #define PG8_WAIT_V(n) asm volatile("s_waitcnt vmcnt(" #n ")" ::: "memory")
; #define PG8_WAIT_L(n) asm volatile("s_waitcnt lgkmcnt(" #n ")" ::: "memory")
; #define PG8_BAR __builtin_amdgcn_s_barrier()
; #define PG8_SCHED __builtin_amdgcn_sched_barrier(0)
; template <class Epi, class Sched, bool ALIGN_EPI>
; __device__ __forceinline__ void gemm_phase(LAS unsigned char* lds, const Gemm g, const Sched& S, const Epi& E) {
;     ...
;             if (last) { vc10 = vn10; vc11 = vn11; }
;             PG8_BWAIT(2); PG8_BCOMMIT(0); PG8_SCHED; PG8_LDA(At, 0, 1); PG8_BISSUE(t + 3 >= nt ? pbn + (size_t)(t + 3 - nt) * 64 * Sched::LDN : pbc + (size_t)(t + 3) * 64 * Sched::LDN); PG8_STAGE_A(PG8_SA(0, 0), vc00, vc01, kb2);
;             PG8_WAIT_V(12); PG8_WAIT_L(0); PG8_BAR; if (half1) { PG8_MMA(1, 0, At, B0); PG8_MMA(1, 1, At, B1); } PG8_BAR; PG8_SCHED;
;             PG8_LDB(B0, 1, 0); PG8_LDB(B1, 1, 1); PG8_SCHED; PG8_LDA(At, 1, 0); PG8_STAGE_A(PG8_SA(0, 1), vc10, vc11, kb2);
.LBB0_4717:
	v_cndmask_b32_e64 v234, v234, v245, s[4:5]
	v_cndmask_b32_e64 v233, v233, v244, s[4:5]
	s_barrier
	v_add_u32_e32 v162, 0x18000, v240
	v_add_u32_e32 v174, 0x1c000, v240
	ds_read_b128 v[178:181], v162
	ds_read_b128 v[182:185], v162 offset:1024
	ds_read_b128 v[186:189], v162 offset:2048
	ds_read_b128 v[190:193], v162 offset:3072
	ds_read_b128 v[162:165], v174
	ds_read_b128 v[166:169], v174 offset:1024
	ds_read_b128 v[170:173], v174 offset:2048
	ds_read_b128 v[174:177], v174 offset:3072
	s_mov_b32 m0, s42
	s_waitcnt lgkmcnt(0)
	ds_read_b128 v[194:197], v241 offset:32768
	ds_read_b128 v[198:201], v241 offset:33792
	ds_read_b128 v[202:205], v241 offset:34816
	ds_read_b128 v[206:209], v241 offset:35840
	ds_read_b128 v[210:213], v241 offset:36864
	ds_read_b128 v[214:217], v241 offset:37888
	ds_read_b128 v[218:221], v241 offset:38912
	ds_read_b128 v[222:225], v241 offset:39936
	global_load_lds_dwordx4 v233, s[26:27]
	s_mov_b32 m0, s43
	s_nop 0
	global_load_lds_dwordx4 v234, s[26:27]
	s_waitcnt vmcnt(12)
	s_waitcnt lgkmcnt(0)
	s_barrier
	s_setprio 1
	s_waitcnt lgkmcnt(0)
	v_mfma_f32_16x16x32_bf16 v[158:161], v[178:181], v[194:197], v[158:161]
	v_mfma_f32_16x16x32_bf16 v[154:157], v[186:189], v[194:197], v[154:157]
	v_mfma_f32_16x16x32_bf16 v[142:145], v[178:181], v[202:205], v[142:145]
	v_mfma_f32_16x16x32_bf16 v[138:141], v[186:189], v[202:205], v[138:141]
	v_mfma_f32_16x16x32_bf16 v[126:129], v[178:181], v[210:213], v[126:129]
	v_mfma_f32_16x16x32_bf16 v[122:125], v[186:189], v[210:213], v[122:125]
	v_mfma_f32_16x16x32_bf16 v[110:113], v[178:181], v[218:221], v[110:113]
	v_mfma_f32_16x16x32_bf16 v[106:109], v[186:189], v[218:221], v[106:109]
	v_mfma_f32_16x16x32_bf16 v[158:161], v[182:185], v[198:201], v[158:161]
	v_mfma_f32_16x16x32_bf16 v[154:157], v[190:193], v[198:201], v[154:157]
	v_mfma_f32_16x16x32_bf16 v[142:145], v[182:185], v[206:209], v[142:145]
	v_mfma_f32_16x16x32_bf16 v[138:141], v[190:193], v[206:209], v[138:141]
	v_mfma_f32_16x16x32_bf16 v[126:129], v[182:185], v[214:217], v[126:129]
	v_mfma_f32_16x16x32_bf16 v[122:125], v[190:193], v[214:217], v[122:125]
	v_mfma_f32_16x16x32_bf16 v[110:113], v[182:185], v[222:225], v[110:113]
	v_mfma_f32_16x16x32_bf16 v[106:109], v[190:193], v[222:225], v[106:109]
	s_setprio 0
	s_setprio 1
	v_mfma_f32_16x16x32_bf16 v[150:153], v[162:165], v[194:197], v[150:153]
	v_mfma_f32_16x16x32_bf16 v[146:149], v[170:173], v[194:197], v[146:149]
	v_mfma_f32_16x16x32_bf16 v[134:137], v[162:165], v[202:205], v[134:137]
	v_mfma_f32_16x16x32_bf16 v[130:133], v[170:173], v[202:205], v[130:133]
	v_mfma_f32_16x16x32_bf16 v[118:121], v[162:165], v[210:213], v[118:121]
	v_mfma_f32_16x16x32_bf16 v[114:117], v[170:173], v[210:213], v[114:117]
	v_mfma_f32_16x16x32_bf16 v[102:105], v[162:165], v[218:221], v[102:105]
	v_mfma_f32_16x16x32_bf16 v[98:101], v[170:173], v[218:221], v[98:101]
	v_mfma_f32_16x16x32_bf16 v[150:153], v[166:169], v[198:201], v[150:153]
	v_mfma_f32_16x16x32_bf16 v[146:149], v[174:177], v[198:201], v[146:149]
	v_mfma_f32_16x16x32_bf16 v[134:137], v[166:169], v[206:209], v[134:137]
	v_mfma_f32_16x16x32_bf16 v[130:133], v[174:177], v[206:209], v[130:133]
	v_mfma_f32_16x16x32_bf16 v[118:121], v[166:169], v[214:217], v[118:121]
	v_mfma_f32_16x16x32_bf16 v[114:117], v[174:177], v[214:217], v[114:117]
	v_mfma_f32_16x16x32_bf16 v[102:105], v[166:169], v[222:225], v[102:105]
	v_mfma_f32_16x16x32_bf16 v[98:101], v[174:177], v[222:225], v[98:101]
	s_setprio 0
	s_barrier
	s_cmp_lt_u32 s54, 12
	s_mov_b64 s[28:29], -1
	s_cbranch_scc0 .LBB0_4719
	s_add_u32 s4, s20, 0x40000
	s_addc_u32 s5, s21, 0
	s_mov_b64 s[28:29], 0

; #define PG8_BWAIT(n) asm volatile("s_waitcnt vmcnt(" #n ")" : "+v"(bv[0]), "+v"(bv[1]), "+v"(bv[2]), "+v"(bv[3]), "+v"(bv[4]), "+v"(bv[5]), "+v"(bv[6]), "+v"(bv[7]) :: "memory")
; #define PG8_STAGE_A(bufoff, V0, V1, kb) do { \
;         __builtin_amdgcn_global_load_lds((const unsigned*)((Abase + (kb)) + (V0)), (LAS unsigned*)(lds + (bufoff) + ldsw), 16, 0, 0); \
;         __builtin_amdgcn_global_load_lds((const unsigned*)((Abase + (kb)) + (V1)), (LAS unsigned*)(lds + (bufoff) + ldsw + 8192), 16, 0, 0); } while (0)
; #define PG8_LDA(dst, b, h) do { _Pragma("unroll") for (int m = 0; m < 4; ++m) _Pragma("unroll") for (int k = 0; k < 2; ++k) dst[m][k] = *(const LAS bf16x8*)(lds + PG8_SA(b, h) + aoff + m * 2048 + k * 1024); } while (0)
; #define PG8_MMA(ai, bj, At, Bt) do { __builtin_amdgcn_s_setprio(1); _Pragma("unroll") for (int m = 0; m < 4; ++m) _Pragma("unroll") for (int n = 0; n < 2; ++n) _Pragma("unroll") for (int k = 0; k < 2; ++k) \
;         acc[ai][bj][m][n] = __builtin_amdgcn_mfma_f32_16x16x32_bf16(Bt[n][k], At[m][k], acc[ai][bj][m][n], 0, 0, 0); __builtin_amdgcn_s_setprio(0); } while (0)
; #define PG8_WAIT_V(n) asm volatile("s_waitcnt vmcnt(" #n ")" ::: "memory")
; #define PG8_WAIT_L(n) asm volatile("s_waitcnt lgkmcnt(" #n ")" ::: "memory")
; #define PG8_BAR __builtin_amdgcn_s_barrier()
; #define PG8_SCHED __builtin_amdgcn_sched_barrier(0)
; template <class Epi, class Sched, bool ALIGN_EPI>
; __device__ __forceinline__ void gemm_phase(LAS unsigned char* lds, const Gemm g, const Sched& S, const Epi& E) {
;     ...
;             PG8_BWAIT(2); PG8_BCOMMIT(1); PG8_SCHED; PG8_LDA(At, 1, 1); PG8_BISSUE(t + 4 >= nt ? pbn + (size_t)(t + 4 - nt) * 64 * Sched::LDN : pbc + (size_t)(t + 4) * 64 * Sched::LDN); PG8_STAGE_A(PG8_SA(1, 0), vc00, vc01, kb2 + 128u);
;             PG8_WAIT_V(12); PG8_WAIT_L(0); PG8_BAR; if (half1) { PG8_MMA(1, 0, At, B0); PG8_MMA(1, 1, At, B1); } PG8_BAR; PG8_SCHED;
.LBB0_4721:
	s_waitcnt vmcnt(2)
	s_nop 0
	v_cvt_pk_bf16_f32 v194, v2, v6
	v_cvt_pk_bf16_f32 v198, v3, v7
	v_cvt_pk_bf16_f32 v202, v4, v8
	v_cvt_pk_bf16_f32 v206, v5, v9
	global_load_dwordx4 v[2:5], v232, s[4:5] offset:0
	global_load_dwordx4 v[6:9], v232, s[4:5] offset:0x400
	v_cvt_pk_bf16_f32 v195, v10, v14
	v_cvt_pk_bf16_f32 v199, v11, v15
	v_cvt_pk_bf16_f32 v203, v12, v16
	v_cvt_pk_bf16_f32 v207, v13, v17
	global_load_dwordx4 v[10:13], v232, s[4:5] offset:0x800
	global_load_dwordx4 v[14:17], v232, s[4:5] offset:0xc00
	v_cvt_pk_bf16_f32 v196, v18, v22
	v_cvt_pk_bf16_f32 v200, v19, v23
	v_cvt_pk_bf16_f32 v204, v20, v24
	v_cvt_pk_bf16_f32 v208, v21, v25
	s_add_u32 s4, s4, 0x1000
	s_addc_u32 s5, s5, 0
	global_load_dwordx4 v[18:21], v232, s[4:5] offset:0
	global_load_dwordx4 v[22:25], v232, s[4:5] offset:0x400
	v_cvt_pk_bf16_f32 v197, v26, v30
	v_cvt_pk_bf16_f32 v201, v27, v31
	v_cvt_pk_bf16_f32 v205, v28, v32
	v_cvt_pk_bf16_f32 v209, v29, v33
	v_lshl_add_u64 v[246:247], s[26:27], 0, v[226:227]
	v_mov_b32_e32 v229, v227
	global_load_dwordx4 v[26:29], v232, s[4:5] offset:0x800
	s_mov_b32 m0, s44
	v_lshl_add_u64 v[248:249], s[26:27], 0, v[228:229]
	global_load_dwordx4 v[30:33], v232, s[4:5] offset:0xc00
	v_add_u32_e32 v210, 0x18000, v235
	v_xor_b32_e32 v211, 64, v210
	v_xor_b32_e32 v212, 0x80, v210
	v_xor_b32_e32 v213, 0xc0, v210
	ds_write_b128 v210, v[194:197]
	ds_write_b128 v211, v[198:201]
	ds_write_b128 v212, v[202:205]
	ds_write_b128 v213, v[206:209]
	ds_read_b128 v[218:221], v241 offset:49152
	ds_read_b128 v[222:225], v241 offset:50176
	ds_read_b128 v[210:213], v241 offset:51200
	ds_read_b128 v[214:217], v241 offset:52224
	ds_read_b128 v[202:205], v241 offset:53248
	ds_read_b128 v[206:209], v241 offset:54272
	ds_read_b128 v[194:197], v241 offset:55296
	ds_read_b128 v[198:201], v241 offset:56320
	v_lshl_add_u64 v[246:247], v[246:247], 0, s[12:13]
	global_load_lds_dwordx4 v[246:247], off
	v_lshl_add_u64 v[246:247], v[248:249], 0, s[12:13]
	s_mov_b32 m0, s45
	s_and_b64 vcc, exec, s[2:3]
	global_load_lds_dwordx4 v[246:247], off
	s_waitcnt vmcnt(12)
	s_waitcnt lgkmcnt(0)
	s_barrier
	s_cbranch_vccnz .LBB0_4723
	s_setprio 1
	s_waitcnt lgkmcnt(0)
	v_mfma_f32_16x16x32_bf16 v[94:97], v[178:181], v[218:221], v[94:97]
	v_mfma_f32_16x16x32_bf16 v[90:93], v[186:189], v[218:221], v[90:93]
	v_mfma_f32_16x16x32_bf16 v[78:81], v[178:181], v[210:213], v[78:81]
	v_mfma_f32_16x16x32_bf16 v[74:77], v[186:189], v[210:213], v[74:77]
	v_mfma_f32_16x16x32_bf16 v[62:65], v[178:181], v[202:205], v[62:65]
	v_mfma_f32_16x16x32_bf16 v[58:61], v[186:189], v[202:205], v[58:61]
	v_mfma_f32_16x16x32_bf16 v[46:49], v[178:181], v[194:197], v[46:49]
	v_mfma_f32_16x16x32_bf16 v[42:45], v[186:189], v[194:197], v[42:45]
	v_mfma_f32_16x16x32_bf16 v[94:97], v[182:185], v[222:225], v[94:97]
	v_mfma_f32_16x16x32_bf16 v[90:93], v[190:193], v[222:225], v[90:93]
	v_mfma_f32_16x16x32_bf16 v[78:81], v[182:185], v[214:217], v[78:81]
	v_mfma_f32_16x16x32_bf16 v[74:77], v[190:193], v[214:217], v[74:77]
	v_mfma_f32_16x16x32_bf16 v[62:65], v[182:185], v[206:209], v[62:65]
	v_mfma_f32_16x16x32_bf16 v[58:61], v[190:193], v[206:209], v[58:61]
	v_mfma_f32_16x16x32_bf16 v[46:49], v[182:185], v[198:201], v[46:49]
	v_mfma_f32_16x16x32_bf16 v[42:45], v[190:193], v[198:201], v[42:45]
	s_setprio 0
	s_setprio 1
	v_mfma_f32_16x16x32_bf16 v[86:89], v[162:165], v[218:221], v[86:89]
	v_mfma_f32_16x16x32_bf16 v[82:85], v[170:173], v[218:221], v[82:85]
	v_mfma_f32_16x16x32_bf16 v[70:73], v[162:165], v[210:213], v[70:73]
	v_mfma_f32_16x16x32_bf16 v[66:69], v[170:173], v[210:213], v[66:69]
	v_mfma_f32_16x16x32_bf16 v[54:57], v[162:165], v[202:205], v[54:57]
	v_mfma_f32_16x16x32_bf16 v[50:53], v[170:173], v[202:205], v[50:53]
	v_mfma_f32_16x16x32_bf16 v[38:41], v[162:165], v[194:197], v[38:41]
	v_mfma_f32_16x16x32_bf16 v[34:37], v[170:173], v[194:197], v[34:37]
	v_mfma_f32_16x16x32_bf16 v[86:89], v[166:169], v[222:225], v[86:89]
	v_mfma_f32_16x16x32_bf16 v[82:85], v[174:177], v[222:225], v[82:85]
	v_mfma_f32_16x16x32_bf16 v[70:73], v[166:169], v[214:217], v[70:73]
	v_mfma_f32_16x16x32_bf16 v[66:69], v[174:177], v[214:217], v[66:69]
	v_mfma_f32_16x16x32_bf16 v[54:57], v[166:169], v[206:209], v[54:57]
	v_mfma_f32_16x16x32_bf16 v[50:53], v[174:177], v[206:209], v[50:53]
	v_mfma_f32_16x16x32_bf16 v[38:41], v[166:169], v[198:201], v[38:41]
	v_mfma_f32_16x16x32_bf16 v[34:37], v[174:177], v[198:201], v[34:37]
	s_setprio 0

; #define PG8_BWAIT(n) asm volatile("s_waitcnt vmcnt(" #n ")" : "+v"(bv[0]), "+v"(bv[1]), "+v"(bv[2]), "+v"(bv[3]), "+v"(bv[4]), "+v"(bv[5]), "+v"(bv[6]), "+v"(bv[7]) :: "memory")
; #define PG8_STAGE_A(bufoff, V0, V1, kb) do { \
;         __builtin_amdgcn_global_load_lds((const unsigned*)((Abase + (kb)) + (V0)), (LAS unsigned*)(lds + (bufoff) + ldsw), 16, 0, 0); \
;         __builtin_amdgcn_global_load_lds((const unsigned*)((Abase + (kb)) + (V1)), (LAS unsigned*)(lds + (bufoff) + ldsw + 8192), 16, 0, 0); } while (0)
; #define PG8_LDA(dst, b, h) do { _Pragma("unroll") for (int m = 0; m < 4; ++m) _Pragma("unroll") for (int k = 0; k < 2; ++k) dst[m][k] = *(const LAS bf16x8*)(lds + PG8_SA(b, h) + aoff + m * 2048 + k * 1024); } while (0)
; #define PG8_LDB(dst, b, h) do { _Pragma("unroll") for (int n = 0; n < 2; ++n) _Pragma("unroll") for (int k = 0; k < 2; ++k) dst[n][k] = *(const LAS bf16x8*)(lds + PG8_SB(b, h) + boff + n * 2048 + k * 1024); } while (0)
; #define PG8_MMA(ai, bj, At, Bt) do { __builtin_amdgcn_s_setprio(1); _Pragma("unroll") for (int m = 0; m < 4; ++m) _Pragma("unroll") for (int n = 0; n < 2; ++n) _Pragma("unroll") for (int k = 0; k < 2; ++k) \
;         acc[ai][bj][m][n] = __builtin_amdgcn_mfma_f32_16x16x32_bf16(Bt[n][k], At[m][k], acc[ai][bj][m][n], 0, 0, 0); __builtin_amdgcn_s_setprio(0); } while (0)
; #define PG8_WAIT_V(n) asm volatile("s_waitcnt vmcnt(" #n ")" ::: "memory")
; #define PG8_WAIT_L(n) asm volatile("s_waitcnt lgkmcnt(" #n ")" ::: "memory")
; #define PG8_BAR __builtin_amdgcn_s_barrier()
; template <class Epi, class Sched, bool ALIGN_EPI>
; __device__ __forceinline__ void gemm_phase(LAS unsigned char* lds, const Gemm g, const Sched& S, const Epi& E) {
;     ...
;             PG8_LDB(B0, 0, 0); PG8_LDB(B1, 0, 1); PG8_SCHED; PG8_LDA(At, 0, 0); PG8_STAGE_A(PG8_SA(1, 1), vc10, vc11, kb1);
;             PG8_WAIT_V(12); PG8_WAIT_L(0); PG8_BAR; PG8_MMA(0, 0, At, B0); PG8_MMA(0, 1, At, B1); PG8_BAR; PG8_SCHED;
;             if (last) { vc10 = vn10; vc11 = vn11; }
;             PG8_BWAIT(2); PG8_BCOMMIT(0); PG8_SCHED; PG8_LDA(At, 0, 1); PG8_BISSUE(t + 3 >= nt ? pbn + (size_t)(t + 3 - nt) * 64 * Sched::LDN : pbc + (size_t)(t + 3) * 64 * Sched::LDN); PG8_STAGE_A(PG8_SA(0, 0), vc00, vc01, kb2);
;             PG8_WAIT_V(12); PG8_WAIT_L(0); PG8_BAR; if (half1) { PG8_MMA(1, 0, At, B0); PG8_MMA(1, 1, At, B1); } PG8_BAR; PG8_SCHED;
.LBB0_4908:
	v_add_u32_e32 v162, 0x10000, v247
	v_add_u32_e32 v174, 0x14000, v247
	ds_read_b128 v[178:181], v162
	ds_read_b128 v[182:185], v162 offset:1024
	ds_read_b128 v[186:189], v162 offset:2048
	ds_read_b128 v[190:193], v162 offset:3072
	ds_read_b128 v[162:165], v174
	ds_read_b128 v[166:169], v174 offset:1024
	ds_read_b128 v[170:173], v174 offset:2048
	ds_read_b128 v[174:177], v174 offset:3072
	s_lshl_b32 s3, s52, 7
	s_add_i32 s2, s3, 0x100
	v_cndmask_b32_e64 v228, v228, v250, s[28:29]
	v_readlane_b32 s56, v254, 53
	v_readlane_b32 s57, v254, 54
	s_add_u32 s30, s56, s3
	s_addc_u32 s31, s57, 0
	v_lshl_add_u64 v[236:237], s[30:31], 0, v[230:231]
	v_lshl_add_u64 v[236:237], v[236:237], 0, s[14:15]
	s_add_i32 m0, s37, 0xc000
	v_mov_b32_e32 v233, v231
	s_waitcnt lgkmcnt(0)
	ds_read_b128 v[194:197], v248
	ds_read_b128 v[198:201], v248 offset:1024
	ds_read_b128 v[202:205], v248 offset:2048
	ds_read_b128 v[206:209], v248 offset:3072
	ds_read_b128 v[210:213], v248 offset:4096
	ds_read_b128 v[214:217], v248 offset:5120
	ds_read_b128 v[218:221], v248 offset:6144
	ds_read_b128 v[222:225], v248 offset:7168
	global_load_lds_dwordx4 v[236:237], off
	v_lshl_add_u64 v[236:237], s[30:31], 0, v[232:233]
	v_lshl_add_u64 v[236:237], v[236:237], 0, s[14:15]
	s_add_i32 m0, s37, 0xe000
	s_nop 0
	global_load_lds_dwordx4 v[236:237], off
	s_waitcnt vmcnt(12)
	s_waitcnt lgkmcnt(0)
	s_barrier
	s_setprio 1
	s_waitcnt lgkmcnt(0)
	v_mfma_f32_16x16x32_bf16 v[158:161], v[178:181], v[194:197], v[158:161]
	v_mfma_f32_16x16x32_bf16 v[154:157], v[186:189], v[194:197], v[154:157]
	v_mfma_f32_16x16x32_bf16 v[142:145], v[178:181], v[202:205], v[142:145]
	v_mfma_f32_16x16x32_bf16 v[138:141], v[186:189], v[202:205], v[138:141]
	v_mfma_f32_16x16x32_bf16 v[126:129], v[178:181], v[210:213], v[126:129]
	v_mfma_f32_16x16x32_bf16 v[122:125], v[186:189], v[210:213], v[122:125]
	v_mfma_f32_16x16x32_bf16 v[110:113], v[178:181], v[218:221], v[110:113]
	v_mfma_f32_16x16x32_bf16 v[106:109], v[186:189], v[218:221], v[106:109]
	v_mfma_f32_16x16x32_bf16 v[158:161], v[182:185], v[198:201], v[158:161]
	v_mfma_f32_16x16x32_bf16 v[154:157], v[190:193], v[198:201], v[154:157]
	v_mfma_f32_16x16x32_bf16 v[142:145], v[182:185], v[206:209], v[142:145]
	v_mfma_f32_16x16x32_bf16 v[138:141], v[190:193], v[206:209], v[138:141]
	v_mfma_f32_16x16x32_bf16 v[126:129], v[182:185], v[214:217], v[126:129]
	v_mfma_f32_16x16x32_bf16 v[122:125], v[190:193], v[214:217], v[122:125]
	v_mfma_f32_16x16x32_bf16 v[110:113], v[182:185], v[222:225], v[110:113]
	v_mfma_f32_16x16x32_bf16 v[106:109], v[190:193], v[222:225], v[106:109]
	s_setprio 0
	s_setprio 1
	v_mfma_f32_16x16x32_bf16 v[150:153], v[162:165], v[194:197], v[150:153]
	v_mfma_f32_16x16x32_bf16 v[146:149], v[170:173], v[194:197], v[146:149]
	v_mfma_f32_16x16x32_bf16 v[134:137], v[162:165], v[202:205], v[134:137]
	v_mfma_f32_16x16x32_bf16 v[130:133], v[170:173], v[202:205], v[130:133]
	v_mfma_f32_16x16x32_bf16 v[118:121], v[162:165], v[210:213], v[118:121]
	v_mfma_f32_16x16x32_bf16 v[114:117], v[170:173], v[210:213], v[114:117]
	v_mfma_f32_16x16x32_bf16 v[102:105], v[162:165], v[218:221], v[102:105]
	v_mfma_f32_16x16x32_bf16 v[98:101], v[170:173], v[218:221], v[98:101]
	v_mfma_f32_16x16x32_bf16 v[150:153], v[166:169], v[198:201], v[150:153]
	v_mfma_f32_16x16x32_bf16 v[146:149], v[174:177], v[198:201], v[146:149]
	v_mfma_f32_16x16x32_bf16 v[134:137], v[166:169], v[206:209], v[134:137]
	v_mfma_f32_16x16x32_bf16 v[130:133], v[174:177], v[206:209], v[130:133]
	v_mfma_f32_16x16x32_bf16 v[118:121], v[166:169], v[214:217], v[118:121]
	v_mfma_f32_16x16x32_bf16 v[114:117], v[174:177], v[214:217], v[114:117]
	v_mfma_f32_16x16x32_bf16 v[102:105], v[166:169], v[222:225], v[102:105]
	v_mfma_f32_16x16x32_bf16 v[98:101], v[174:177], v[222:225], v[98:101]
	s_setprio 0
	s_barrier
	s_add_i32 s8, s52, -1
	s_lshl_b64 s[30:31], s[8:9], 18
	s_add_u32 s3, s49, s30
	s_addc_u32 s8, s21, s31
	s_and_b64 s[30:31], s[26:27], exec
	s_cselect_b32 s30, s50, s3
	s_cselect_b32 s31, s51, s8
	s_add_u32 s54, s30, 0x1000
	s_waitcnt vmcnt(2)
	v_cndmask_b32_e64 v226, v226, v249, s[28:29]
	v_cvt_pk_bf16_f32 v194, v2, v6
	v_cvt_pk_bf16_f32 v198, v3, v7
	v_cvt_pk_bf16_f32 v202, v4, v8
	v_cvt_pk_bf16_f32 v206, v5, v9
	global_load_dwordx4 v[2:5], v240, s[30:31] offset:0
	s_addc_u32 s55, s31, 0
	global_load_dwordx4 v[6:9], v240, s[54:55] offset:0
	v_cvt_pk_bf16_f32 v195, v10, v14
	v_cvt_pk_bf16_f32 v199, v11, v15
	v_cvt_pk_bf16_f32 v203, v12, v16
	v_cvt_pk_bf16_f32 v207, v13, v17
	s_add_u32 s54, s30, 0x2000
	s_addc_u32 s55, s31, 0
	global_load_dwordx4 v[10:13], v240, s[54:55] offset:0
	s_add_u32 s54, s30, 0x3000
	s_addc_u32 s55, s31, 0
	global_load_dwordx4 v[14:17], v240, s[54:55] offset:0
	v_cvt_pk_bf16_f32 v196, v18, v22
	v_cvt_pk_bf16_f32 v200, v19, v23
	v_cvt_pk_bf16_f32 v204, v20, v24
	v_cvt_pk_bf16_f32 v208, v21, v25
	s_add_u32 s54, s30, 0x4000
	s_addc_u32 s55, s31, 0
	global_load_dwordx4 v[18:21], v240, s[54:55] offset:0
	s_add_u32 s54, s30, 0x5000
	s_addc_u32 s55, s31, 0
	global_load_dwordx4 v[22:25], v240, s[54:55] offset:0
	v_cvt_pk_bf16_f32 v197, v26, v30
	v_cvt_pk_bf16_f32 v201, v27, v31
	v_cvt_pk_bf16_f32 v205, v28, v32
	v_cvt_pk_bf16_f32 v209, v29, v33
	s_add_u32 s54, s30, 0x6000
	s_addc_u32 s55, s31, 0
	s_add_u32 s30, s30, 0x7000
	global_load_dwordx4 v[26:29], v240, s[54:55] offset:0
	s_addc_u32 s31, s31, 0
	global_load_dwordx4 v[30:33], v240, s[30:31] offset:0
	v_add_u32_e32 v210, 0x10000, v242
	v_xor_b32_e32 v211, 64, v210
	v_xor_b32_e32 v212, 0x80, v210
	v_xor_b32_e32 v213, 0xc0, v210
	ds_write_b128 v210, v[194:197]
	ds_write_b128 v211, v[198:201]
	ds_write_b128 v212, v[202:205]
	ds_write_b128 v213, v[206:209]
	ds_read_b128 v[218:221], v248 offset:16384
	ds_read_b128 v[222:225], v248 offset:17408
	ds_read_b128 v[210:213], v248 offset:18432
	ds_read_b128 v[214:217], v248 offset:19456
	ds_read_b128 v[202:205], v248 offset:20480
	ds_read_b128 v[206:209], v248 offset:21504
	ds_read_b128 v[194:197], v248 offset:22528
	ds_read_b128 v[198:201], v248 offset:23552
	s_and_b64 s[30:31], s[28:29], exec
	s_cselect_b32 s2, 0, s2
	s_cselect_b32 s3, 0, 0
	s_add_u32 s30, s56, s2
	s_mov_b32 m0, s37
	s_addc_u32 s31, s57, s3
	global_load_lds_dwordx4 v226, s[30:31]
	s_mov_b32 m0, s38
	v_mov_b32_e32 v227, v231
	global_load_lds_dwordx4 v228, s[30:31]
	s_waitcnt vmcnt(12)
	s_waitcnt lgkmcnt(0)
	v_lshl_add_u64 v[238:239], s[30:31], 0, v[226:227]
	v_mov_b32_e32 v229, v231
	v_cndmask_b32_e64 v227, 0, 1, s[24:25]
	v_lshl_add_u64 v[236:237], s[30:31], 0, v[228:229]
	v_cmp_ne_u32_e64 s[2:3], 1, v227
	s_andn2_b64 vcc, exec, s[24:25]
	s_barrier
; #define PG8_STAGE_A(bufoff, V0, V1, kb) do { \
;         __builtin_amdgcn_global_load_lds((const unsigned*)((Abase + (kb)) + (V0)), (LAS unsigned*)(lds + (bufoff) + ldsw), 16, 0, 0); \
;         __builtin_amdgcn_global_load_lds((const unsigned*)((Abase + (kb)) + (V1)), (LAS unsigned*)(lds + (bufoff) + ldsw + 8192), 16, 0, 0); } while (0)
; #define PG8_LDA(dst, b, h) do { _Pragma("unroll") for (int m = 0; m < 4; ++m) _Pragma("unroll") for (int k = 0; k < 2; ++k) dst[m][k] = *(const LAS bf16x8*)(lds + PG8_SA(b, h) + aoff + m * 2048 + k * 1024); } while (0)
; #define PG8_LDB(dst, b, h) do { _Pragma("unroll") for (int n = 0; n < 2; ++n) _Pragma("unroll") for (int k = 0; k < 2; ++k) dst[n][k] = *(const LAS bf16x8*)(lds + PG8_SB(b, h) + boff + n * 2048 + k * 1024); } while (0)
; #define PG8_MMA(ai, bj, At, Bt) do { __builtin_amdgcn_s_setprio(1); _Pragma("unroll") for (int m = 0; m < 4; ++m) _Pragma("unroll") for (int n = 0; n < 2; ++n) _Pragma("unroll") for (int k = 0; k < 2; ++k) \
;         acc[ai][bj][m][n] = __builtin_amdgcn_mfma_f32_16x16x32_bf16(Bt[n][k], At[m][k], acc[ai][bj][m][n], 0, 0, 0); __builtin_amdgcn_s_setprio(0); } while (0)
; #define PG8_WAIT_V(n) asm volatile("s_waitcnt vmcnt(" #n ")" ::: "memory")
; #define PG8_WAIT_L(n) asm volatile("s_waitcnt lgkmcnt(" #n ")" ::: "memory")
; #define PG8_BAR __builtin_amdgcn_s_barrier()
; #define PG8_SCHED __builtin_amdgcn_sched_barrier(0)
; template <class Epi, class Sched, bool ALIGN_EPI>
; __device__ __forceinline__ void gemm_phase(LAS unsigned char* lds, const Gemm g, const Sched& S, const Epi& E) {
;     ...
;             PG8_WAIT_V(12); PG8_WAIT_L(0); PG8_BAR; if (half1) { PG8_MMA(1, 0, At, B0); PG8_MMA(1, 1, At, B1); } PG8_BAR; PG8_SCHED;
;             PG8_LDB(B0, 1, 0); PG8_LDB(B1, 1, 1); PG8_SCHED; PG8_LDA(At, 1, 0); PG8_STAGE_A(PG8_SA(0, 1), vc10, vc11, kb2);
;             PG8_WAIT_V(12); PG8_WAIT_L(0); PG8_BAR; PG8_MMA(0, 0, At, B0); PG8_MMA(0, 1, At, B1); PG8_BAR; PG8_SCHED;
	s_cbranch_vccnz .LBB0_4910
	s_setprio 1
	s_waitcnt lgkmcnt(0)
	v_mfma_f32_16x16x32_bf16 v[94:97], v[178:181], v[218:221], v[94:97]
	v_mfma_f32_16x16x32_bf16 v[90:93], v[186:189], v[218:221], v[90:93]
	v_mfma_f32_16x16x32_bf16 v[78:81], v[178:181], v[210:213], v[78:81]
	v_mfma_f32_16x16x32_bf16 v[74:77], v[186:189], v[210:213], v[74:77]
	v_mfma_f32_16x16x32_bf16 v[62:65], v[178:181], v[202:205], v[62:65]
	v_mfma_f32_16x16x32_bf16 v[58:61], v[186:189], v[202:205], v[58:61]
	v_mfma_f32_16x16x32_bf16 v[46:49], v[178:181], v[194:197], v[46:49]
	v_mfma_f32_16x16x32_bf16 v[42:45], v[186:189], v[194:197], v[42:45]
	v_mfma_f32_16x16x32_bf16 v[94:97], v[182:185], v[222:225], v[94:97]
	v_mfma_f32_16x16x32_bf16 v[90:93], v[190:193], v[222:225], v[90:93]
	v_mfma_f32_16x16x32_bf16 v[78:81], v[182:185], v[214:217], v[78:81]
	v_mfma_f32_16x16x32_bf16 v[74:77], v[190:193], v[214:217], v[74:77]
	v_mfma_f32_16x16x32_bf16 v[62:65], v[182:185], v[206:209], v[62:65]
	v_mfma_f32_16x16x32_bf16 v[58:61], v[190:193], v[206:209], v[58:61]
	v_mfma_f32_16x16x32_bf16 v[46:49], v[182:185], v[198:201], v[46:49]
	v_mfma_f32_16x16x32_bf16 v[42:45], v[190:193], v[198:201], v[42:45]
	s_setprio 0
	s_setprio 1
	v_mfma_f32_16x16x32_bf16 v[86:89], v[162:165], v[218:221], v[86:89]
	v_mfma_f32_16x16x32_bf16 v[82:85], v[170:173], v[218:221], v[82:85]
	v_mfma_f32_16x16x32_bf16 v[70:73], v[162:165], v[210:213], v[70:73]
	v_mfma_f32_16x16x32_bf16 v[66:69], v[170:173], v[210:213], v[66:69]
	v_mfma_f32_16x16x32_bf16 v[54:57], v[162:165], v[202:205], v[54:57]
	v_mfma_f32_16x16x32_bf16 v[50:53], v[170:173], v[202:205], v[50:53]
	v_mfma_f32_16x16x32_bf16 v[38:41], v[162:165], v[194:197], v[38:41]
	v_mfma_f32_16x16x32_bf16 v[34:37], v[170:173], v[194:197], v[34:37]
	v_mfma_f32_16x16x32_bf16 v[86:89], v[166:169], v[222:225], v[86:89]
	v_mfma_f32_16x16x32_bf16 v[82:85], v[174:177], v[222:225], v[82:85]
	v_mfma_f32_16x16x32_bf16 v[70:73], v[166:169], v[214:217], v[70:73]
	v_mfma_f32_16x16x32_bf16 v[66:69], v[174:177], v[214:217], v[66:69]
	v_mfma_f32_16x16x32_bf16 v[54:57], v[166:169], v[206:209], v[54:57]
	v_mfma_f32_16x16x32_bf16 v[50:53], v[174:177], v[206:209], v[50:53]
	v_mfma_f32_16x16x32_bf16 v[38:41], v[166:169], v[198:201], v[38:41]
	v_mfma_f32_16x16x32_bf16 v[34:37], v[174:177], v[198:201], v[34:37]
	s_setprio 0
.LBB0_4910:
	v_cndmask_b32_e64 v232, v232, v252, s[28:29]
	v_cndmask_b32_e64 v230, v230, v251, s[28:29]
	s_barrier
	v_add_u32_e32 v162, 0x18000, v247
	v_add_u32_e32 v174, 0x1c000, v247
	ds_read_b128 v[178:181], v162
	ds_read_b128 v[182:185], v162 offset:1024
	ds_read_b128 v[186:189], v162 offset:2048
	ds_read_b128 v[190:193], v162 offset:3072
	ds_read_b128 v[162:165], v174
	ds_read_b128 v[166:169], v174 offset:1024
	ds_read_b128 v[170:173], v174 offset:2048
	ds_read_b128 v[174:177], v174 offset:3072
	s_mov_b32 m0, s39
	s_waitcnt lgkmcnt(0)
	ds_read_b128 v[194:197], v248 offset:32768
	ds_read_b128 v[198:201], v248 offset:33792
	ds_read_b128 v[202:205], v248 offset:34816
	ds_read_b128 v[206:209], v248 offset:35840
	ds_read_b128 v[210:213], v248 offset:36864
	ds_read_b128 v[214:217], v248 offset:37888
	ds_read_b128 v[218:221], v248 offset:38912
	ds_read_b128 v[222:225], v248 offset:39936
	global_load_lds_dwordx4 v230, s[30:31]
	s_mov_b32 m0, s40
	s_nop 0
	global_load_lds_dwordx4 v232, s[30:31]
	s_waitcnt vmcnt(12)
	s_waitcnt lgkmcnt(0)
	s_barrier
	s_setprio 1
	s_waitcnt lgkmcnt(0)
	v_mfma_f32_16x16x32_bf16 v[158:161], v[178:181], v[194:197], v[158:161]
	v_mfma_f32_16x16x32_bf16 v[154:157], v[186:189], v[194:197], v[154:157]
	v_mfma_f32_16x16x32_bf16 v[142:145], v[178:181], v[202:205], v[142:145]
	v_mfma_f32_16x16x32_bf16 v[138:141], v[186:189], v[202:205], v[138:141]
	v_mfma_f32_16x16x32_bf16 v[126:129], v[178:181], v[210:213], v[126:129]
	v_mfma_f32_16x16x32_bf16 v[122:125], v[186:189], v[210:213], v[122:125]
	v_mfma_f32_16x16x32_bf16 v[110:113], v[178:181], v[218:221], v[110:113]
	v_mfma_f32_16x16x32_bf16 v[106:109], v[186:189], v[218:221], v[106:109]
	v_mfma_f32_16x16x32_bf16 v[158:161], v[182:185], v[198:201], v[158:161]
	v_mfma_f32_16x16x32_bf16 v[154:157], v[190:193], v[198:201], v[154:157]
	v_mfma_f32_16x16x32_bf16 v[142:145], v[182:185], v[206:209], v[142:145]
	v_mfma_f32_16x16x32_bf16 v[138:141], v[190:193], v[206:209], v[138:141]
	v_mfma_f32_16x16x32_bf16 v[126:129], v[182:185], v[214:217], v[126:129]
	v_mfma_f32_16x16x32_bf16 v[122:125], v[190:193], v[214:217], v[122:125]
	v_mfma_f32_16x16x32_bf16 v[110:113], v[182:185], v[222:225], v[110:113]
	v_mfma_f32_16x16x32_bf16 v[106:109], v[190:193], v[222:225], v[106:109]
	s_setprio 0
	s_setprio 1
	v_mfma_f32_16x16x32_bf16 v[150:153], v[162:165], v[194:197], v[150:153]
	v_mfma_f32_16x16x32_bf16 v[146:149], v[170:173], v[194:197], v[146:149]
	v_mfma_f32_16x16x32_bf16 v[134:137], v[162:165], v[202:205], v[134:137]
	v_mfma_f32_16x16x32_bf16 v[130:133], v[170:173], v[202:205], v[130:133]
	v_mfma_f32_16x16x32_bf16 v[118:121], v[162:165], v[210:213], v[118:121]
	v_mfma_f32_16x16x32_bf16 v[114:117], v[170:173], v[210:213], v[114:117]
	v_mfma_f32_16x16x32_bf16 v[102:105], v[162:165], v[218:221], v[102:105]
	v_mfma_f32_16x16x32_bf16 v[98:101], v[170:173], v[218:221], v[98:101]
	v_mfma_f32_16x16x32_bf16 v[150:153], v[166:169], v[198:201], v[150:153]
	v_mfma_f32_16x16x32_bf16 v[146:149], v[174:177], v[198:201], v[146:149]
	v_mfma_f32_16x16x32_bf16 v[134:137], v[166:169], v[206:209], v[134:137]
	v_mfma_f32_16x16x32_bf16 v[130:133], v[174:177], v[206:209], v[130:133]
	v_mfma_f32_16x16x32_bf16 v[118:121], v[166:169], v[214:217], v[118:121]
	v_mfma_f32_16x16x32_bf16 v[114:117], v[174:177], v[214:217], v[114:117]
	v_mfma_f32_16x16x32_bf16 v[102:105], v[166:169], v[222:225], v[102:105]
	v_mfma_f32_16x16x32_bf16 v[98:101], v[174:177], v[222:225], v[98:101]
	s_setprio 0
	s_barrier
; #define PG8_BWAIT(n) asm volatile("s_waitcnt vmcnt(" #n ")" : "+v"(bv[0]), "+v"(bv[1]), "+v"(bv[2]), "+v"(bv[3]), "+v"(bv[4]), "+v"(bv[5]), "+v"(bv[6]), "+v"(bv[7]) :: "memory")
; #define PG8_STAGE_A(bufoff, V0, V1, kb) do { \
;         __builtin_amdgcn_global_load_lds((const unsigned*)((Abase + (kb)) + (V0)), (LAS unsigned*)(lds + (bufoff) + ldsw), 16, 0, 0); \
;         __builtin_amdgcn_global_load_lds((const unsigned*)((Abase + (kb)) + (V1)), (LAS unsigned*)(lds + (bufoff) + ldsw + 8192), 16, 0, 0); } while (0)
; #define PG8_LDA(dst, b, h) do { _Pragma("unroll") for (int m = 0; m < 4; ++m) _Pragma("unroll") for (int k = 0; k < 2; ++k) dst[m][k] = *(const LAS bf16x8*)(lds + PG8_SA(b, h) + aoff + m * 2048 + k * 1024); } while (0)
; #define PG8_MMA(ai, bj, At, Bt) do { __builtin_amdgcn_s_setprio(1); _Pragma("unroll") for (int m = 0; m < 4; ++m) _Pragma("unroll") for (int n = 0; n < 2; ++n) _Pragma("unroll") for (int k = 0; k < 2; ++k) \
;         acc[ai][bj][m][n] = __builtin_amdgcn_mfma_f32_16x16x32_bf16(Bt[n][k], At[m][k], acc[ai][bj][m][n], 0, 0, 0); __builtin_amdgcn_s_setprio(0); } while (0)
; #define PG8_WAIT_V(n) asm volatile("s_waitcnt vmcnt(" #n ")" ::: "memory")
; #define PG8_WAIT_L(n) asm volatile("s_waitcnt lgkmcnt(" #n ")" ::: "memory")
; #define PG8_BAR __builtin_amdgcn_s_barrier()
; #define PG8_SCHED __builtin_amdgcn_sched_barrier(0)
; template <class Epi, class Sched, bool ALIGN_EPI>
; __device__ __forceinline__ void gemm_phase(LAS unsigned char* lds, const Gemm g, const Sched& S, const Epi& E) {
;     ...
;             PG8_BWAIT(2); PG8_BCOMMIT(1); PG8_SCHED; PG8_LDA(At, 1, 1); PG8_BISSUE(t + 4 >= nt ? pbn + (size_t)(t + 4 - nt) * 64 * Sched::LDN : pbc + (size_t)(t + 4) * 64 * Sched::LDN); PG8_STAGE_A(PG8_SA(1, 0), vc00, vc01, kb2 + 128u);
;             PG8_WAIT_V(12); PG8_WAIT_L(0); PG8_BAR; if (half1) { PG8_MMA(1, 0, At, B0); PG8_MMA(1, 1, At, B1); } PG8_BAR; PG8_SCHED;
	s_lshl_b32 s8, s52, 16
	s_lshl_b64 s[28:29], s[8:9], 2
	s_add_u32 s28, s49, s28
	s_addc_u32 s29, s21, s29
	s_add_u32 s30, s28, 0x1000
	s_waitcnt vmcnt(2)
	s_nop 0
	v_cvt_pk_bf16_f32 v194, v2, v6
	v_cvt_pk_bf16_f32 v198, v3, v7
	v_cvt_pk_bf16_f32 v202, v4, v8
	v_cvt_pk_bf16_f32 v206, v5, v9
	global_load_dwordx4 v[2:5], v240, s[28:29] offset:0
	s_addc_u32 s31, s29, 0
	global_load_dwordx4 v[6:9], v240, s[30:31] offset:0
	v_cvt_pk_bf16_f32 v195, v10, v14
	v_cvt_pk_bf16_f32 v199, v11, v15
	v_cvt_pk_bf16_f32 v203, v12, v16
	v_cvt_pk_bf16_f32 v207, v13, v17
	s_add_u32 s30, s28, 0x2000
	s_addc_u32 s31, s29, 0
	global_load_dwordx4 v[10:13], v240, s[30:31] offset:0
	s_add_u32 s30, s28, 0x3000
	s_addc_u32 s31, s29, 0
	global_load_dwordx4 v[14:17], v240, s[30:31] offset:0
	v_cvt_pk_bf16_f32 v196, v18, v22
	v_cvt_pk_bf16_f32 v200, v19, v23
	v_cvt_pk_bf16_f32 v204, v20, v24
	v_cvt_pk_bf16_f32 v208, v21, v25
	s_add_u32 s30, s28, 0x4000
	s_addc_u32 s31, s29, 0
	global_load_dwordx4 v[18:21], v240, s[30:31] offset:0
	s_add_u32 s30, s28, 0x5000
	s_addc_u32 s31, s29, 0
	global_load_dwordx4 v[22:25], v240, s[30:31] offset:0
	v_cvt_pk_bf16_f32 v197, v26, v30
	v_cvt_pk_bf16_f32 v201, v27, v31
	v_cvt_pk_bf16_f32 v205, v28, v32
	v_cvt_pk_bf16_f32 v209, v29, v33
	s_add_u32 s30, s28, 0x6000
	s_addc_u32 s31, s29, 0
	global_load_dwordx4 v[26:29], v240, s[30:31] offset:0
	s_add_u32 s28, s28, 0x7000
	s_mov_b32 m0, s41
	s_addc_u32 s29, s29, 0
	global_load_dwordx4 v[30:33], v240, s[28:29] offset:0
	v_add_u32_e32 v210, 0x18000, v242
	v_xor_b32_e32 v211, 64, v210
	v_xor_b32_e32 v212, 0x80, v210
	v_xor_b32_e32 v213, 0xc0, v210
	ds_write_b128 v210, v[194:197]
	ds_write_b128 v211, v[198:201]
	ds_write_b128 v212, v[202:205]
	ds_write_b128 v213, v[206:209]
	ds_read_b128 v[218:221], v248 offset:49152
	ds_read_b128 v[222:225], v248 offset:50176
	ds_read_b128 v[210:213], v248 offset:51200
	ds_read_b128 v[214:217], v248 offset:52224
	ds_read_b128 v[202:205], v248 offset:53248
	ds_read_b128 v[206:209], v248 offset:54272
	ds_read_b128 v[194:197], v248 offset:55296
	ds_read_b128 v[198:201], v248 offset:56320
	v_lshl_add_u64 v[238:239], v[238:239], 0, s[14:15]
	global_load_lds_dwordx4 v[238:239], off
	v_lshl_add_u64 v[236:237], v[236:237], 0, s[14:15]
	s_mov_b32 m0, s42
	s_and_b64 vcc, exec, s[2:3]
	global_load_lds_dwordx4 v[236:237], off
	s_waitcnt vmcnt(12)
	s_waitcnt lgkmcnt(0)
	s_barrier
	s_cbranch_vccnz .LBB0_4907
	s_setprio 1
	s_waitcnt lgkmcnt(0)
	v_mfma_f32_16x16x32_bf16 v[94:97], v[178:181], v[218:221], v[94:97]
	v_mfma_f32_16x16x32_bf16 v[90:93], v[186:189], v[218:221], v[90:93]
	v_mfma_f32_16x16x32_bf16 v[78:81], v[178:181], v[210:213], v[78:81]
	v_mfma_f32_16x16x32_bf16 v[74:77], v[186:189], v[210:213], v[74:77]
	v_mfma_f32_16x16x32_bf16 v[62:65], v[178:181], v[202:205], v[62:65]
	v_mfma_f32_16x16x32_bf16 v[58:61], v[186:189], v[202:205], v[58:61]
	v_mfma_f32_16x16x32_bf16 v[46:49], v[178:181], v[194:197], v[46:49]
	v_mfma_f32_16x16x32_bf16 v[42:45], v[186:189], v[194:197], v[42:45]
	v_mfma_f32_16x16x32_bf16 v[94:97], v[182:185], v[222:225], v[94:97]
	v_mfma_f32_16x16x32_bf16 v[90:93], v[190:193], v[222:225], v[90:93]
	v_mfma_f32_16x16x32_bf16 v[78:81], v[182:185], v[214:217], v[78:81]
	v_mfma_f32_16x16x32_bf16 v[74:77], v[190:193], v[214:217], v[74:77]
	v_mfma_f32_16x16x32_bf16 v[62:65], v[182:185], v[206:209], v[62:65]
	v_mfma_f32_16x16x32_bf16 v[58:61], v[190:193], v[206:209], v[58:61]
	v_mfma_f32_16x16x32_bf16 v[46:49], v[182:185], v[198:201], v[46:49]
	v_mfma_f32_16x16x32_bf16 v[42:45], v[190:193], v[198:201], v[42:45]
	s_setprio 0
	s_setprio 1
	v_mfma_f32_16x16x32_bf16 v[86:89], v[162:165], v[218:221], v[86:89]
	v_mfma_f32_16x16x32_bf16 v[82:85], v[170:173], v[218:221], v[82:85]
	v_mfma_f32_16x16x32_bf16 v[70:73], v[162:165], v[210:213], v[70:73]
	v_mfma_f32_16x16x32_bf16 v[66:69], v[170:173], v[210:213], v[66:69]
	v_mfma_f32_16x16x32_bf16 v[54:57], v[162:165], v[202:205], v[54:57]
	v_mfma_f32_16x16x32_bf16 v[50:53], v[170:173], v[202:205], v[50:53]
	v_mfma_f32_16x16x32_bf16 v[38:41], v[162:165], v[194:197], v[38:41]
	v_mfma_f32_16x16x32_bf16 v[34:37], v[170:173], v[194:197], v[34:37]
	v_mfma_f32_16x16x32_bf16 v[86:89], v[166:169], v[222:225], v[86:89]
	v_mfma_f32_16x16x32_bf16 v[82:85], v[174:177], v[222:225], v[82:85]
	v_mfma_f32_16x16x32_bf16 v[70:73], v[166:169], v[214:217], v[70:73]
	v_mfma_f32_16x16x32_bf16 v[66:69], v[174:177], v[214:217], v[66:69]
	v_mfma_f32_16x16x32_bf16 v[54:57], v[166:169], v[206:209], v[54:57]
	v_mfma_f32_16x16x32_bf16 v[50:53], v[174:177], v[206:209], v[50:53]
	v_mfma_f32_16x16x32_bf16 v[38:41], v[166:169], v[198:201], v[38:41]
	v_mfma_f32_16x16x32_bf16 v[34:37], v[174:177], v[198:201], v[34:37]
	s_setprio 0
	s_branch .LBB0_4907
